# on top of the XCD-contiguous MoE order: one static s_setprio 1 for waves 4-7 in front of five GEMM K-loops (P1, P7, P8, P9, P14), hipcc's per-segment priority flips inside those loops deleted
# speedup vs baseline: 1.0132x; 1.0132x over previous
.LBB0_129:
	s_add_u32 s14, s38, 0x100
	s_addc_u32 s15, s39, 0
	s_add_u32 s38, s42, 0x80
	v_mov_b32_e32 v2, 0
	s_addc_u32 s39, s43, 0
	s_mov_b32 s29, -2
	v_mov_b32_e32 v3, v2
	v_mov_b32_e32 v4, v2
	v_mov_b32_e32 v5, v2
	v_mov_b32_e32 v6, v2
	v_mov_b32_e32 v7, v2
	v_mov_b32_e32 v8, v2
	v_mov_b32_e32 v9, v2
	v_mov_b32_e32 v14, v2
	v_mov_b32_e32 v15, v2
	v_mov_b32_e32 v16, v2
	v_mov_b32_e32 v17, v2
	v_mov_b32_e32 v22, v2
	v_mov_b32_e32 v23, v2
	v_mov_b32_e32 v24, v2
	v_mov_b32_e32 v25, v2
	v_mov_b32_e32 v30, v2
	v_mov_b32_e32 v31, v2
	v_mov_b32_e32 v32, v2
	v_mov_b32_e32 v33, v2
	v_mov_b32_e32 v40, v2
	v_mov_b32_e32 v41, v2
	v_mov_b32_e32 v42, v2
	v_mov_b32_e32 v43, v2
	v_mov_b32_e32 v48, v2
	v_mov_b32_e32 v49, v2
	v_mov_b32_e32 v50, v2
	v_mov_b32_e32 v51, v2
	v_mov_b32_e32 v56, v2
	v_mov_b32_e32 v57, v2
	v_mov_b32_e32 v58, v2
	v_mov_b32_e32 v59, v2
	v_mov_b32_e32 v10, v2
	v_mov_b32_e32 v11, v2
	v_mov_b32_e32 v12, v2
	v_mov_b32_e32 v13, v2
	v_mov_b32_e32 v18, v2
	v_mov_b32_e32 v19, v2
	v_mov_b32_e32 v20, v2
	v_mov_b32_e32 v21, v2
	v_mov_b32_e32 v26, v2
	v_mov_b32_e32 v27, v2
	v_mov_b32_e32 v28, v2
	v_mov_b32_e32 v29, v2
	v_mov_b32_e32 v36, v2
	v_mov_b32_e32 v37, v2
	v_mov_b32_e32 v38, v2
	v_mov_b32_e32 v39, v2
	v_mov_b32_e32 v44, v2
	v_mov_b32_e32 v45, v2
	v_mov_b32_e32 v46, v2
	v_mov_b32_e32 v47, v2
	v_mov_b32_e32 v52, v2
	v_mov_b32_e32 v53, v2
	v_mov_b32_e32 v54, v2
	v_mov_b32_e32 v55, v2
	v_mov_b32_e32 v60, v2
	v_mov_b32_e32 v61, v2
	v_mov_b32_e32 v62, v2
	v_mov_b32_e32 v63, v2
	v_mov_b32_e32 v64, v2
	v_mov_b32_e32 v65, v2
	v_mov_b32_e32 v66, v2
	v_mov_b32_e32 v67, v2
	v_mov_b32_e32 v68, v2
	v_mov_b32_e32 v69, v2
	v_mov_b32_e32 v70, v2
	v_mov_b32_e32 v71, v2
	v_mov_b32_e32 v72, v2
	v_mov_b32_e32 v73, v2
	v_mov_b32_e32 v74, v2
	v_mov_b32_e32 v75, v2
	v_mov_b32_e32 v76, v2
	v_mov_b32_e32 v77, v2
	v_mov_b32_e32 v78, v2
	v_mov_b32_e32 v79, v2
	v_mov_b32_e32 v84, v2
	v_mov_b32_e32 v85, v2
	v_mov_b32_e32 v86, v2
	v_mov_b32_e32 v87, v2
	v_mov_b32_e32 v92, v2
	v_mov_b32_e32 v93, v2
	v_mov_b32_e32 v94, v2
	v_mov_b32_e32 v95, v2
	v_mov_b32_e32 v100, v2
	v_mov_b32_e32 v101, v2
	v_mov_b32_e32 v102, v2
	v_mov_b32_e32 v103, v2
	v_mov_b32_e32 v108, v2
	v_mov_b32_e32 v109, v2
	v_mov_b32_e32 v110, v2
	v_mov_b32_e32 v111, v2
	v_mov_b32_e32 v116, v2
	v_mov_b32_e32 v117, v2
	v_mov_b32_e32 v118, v2
	v_mov_b32_e32 v119, v2
	v_mov_b32_e32 v80, v2
	v_mov_b32_e32 v81, v2
	v_mov_b32_e32 v82, v2
	v_mov_b32_e32 v83, v2
	v_mov_b32_e32 v88, v2
	v_mov_b32_e32 v89, v2
	v_mov_b32_e32 v90, v2
	v_mov_b32_e32 v91, v2
	v_mov_b32_e32 v96, v2
	v_mov_b32_e32 v97, v2
	v_mov_b32_e32 v98, v2
	v_mov_b32_e32 v99, v2
	v_mov_b32_e32 v104, v2
	v_mov_b32_e32 v105, v2
	v_mov_b32_e32 v106, v2
	v_mov_b32_e32 v107, v2
	v_mov_b32_e32 v112, v2
	v_mov_b32_e32 v113, v2
	v_mov_b32_e32 v114, v2
	v_mov_b32_e32 v115, v2
	v_mov_b32_e32 v120, v2
	v_mov_b32_e32 v121, v2
	v_mov_b32_e32 v122, v2
	v_mov_b32_e32 v123, v2
	v_mov_b32_e32 v124, v2
	v_mov_b32_e32 v125, v2
	v_mov_b32_e32 v126, v2
	v_mov_b32_e32 v127, v2
	v_mov_b32_e32 v128, v2
	v_mov_b32_e32 v129, v2
	v_mov_b32_e32 v130, v2
	v_mov_b32_e32 v131, v2
	v_readfirstlane_b32 s96, v0
	s_nop 3
	s_bitcmp1_b32 s96, 8
	s_cbranch_scc0 .Lsp130
	s_setprio 1
.Lsp130:
.LBB0_130:
	s_add_u32 s4, s38, 0x80
	s_addc_u32 s5, s39, 0
	s_add_i32 s31, 0, 0x10000
	s_cmp_eq_u32 s29, 28
	s_cselect_b32 s5, s35, s5
	s_cselect_b32 s4, s34, s4
	v_add_u32_e32 v146, s31, v148
	s_cselect_b32 s43, s37, s15
	s_cselect_b32 s42, s36, s14
	s_add_i32 s68, 0, 0x14000
	ds_read_b128 v[152:155], v146
	ds_read_b128 v[156:159], v146 offset:1024
	ds_read_b128 v[160:163], v146 offset:2048
	ds_read_b128 v[164:167], v146 offset:3072
	v_add_u32_e32 v146, s68, v148
	ds_read_b128 v[168:171], v146
	ds_read_b128 v[172:175], v146 offset:1024
	ds_read_b128 v[176:179], v146 offset:2048
	ds_read_b128 v[180:183], v146 offset:3072
	v_lshl_add_u64 v[146:147], s[38:39], 0, v[144:145]
	s_add_i32 m0, s48, 0xc000
	ds_read_b128 v[184:187], v150
	ds_read_b128 v[188:191], v150 offset:1024
	ds_read_b128 v[192:195], v150 offset:2048
	ds_read_b128 v[196:199], v150 offset:3072
	ds_read_b128 v[224:227], v150 offset:4096
	ds_read_b128 v[228:231], v150 offset:5120
	ds_read_b128 v[238:241], v150 offset:6144
	ds_read_b128 v[242:245], v150 offset:7168
	global_load_lds_dwordx4 v[146:147], off
	v_lshl_add_u64 v[146:147], s[38:39], 0, v[142:143]
	s_add_i32 m0, s48, 0xe000
	s_nop 0
	global_load_lds_dwordx4 v[146:147], off
	s_waitcnt vmcnt(8)
	s_waitcnt lgkmcnt(0)
	s_barrier
	s_waitcnt lgkmcnt(0)
	v_mfma_f32_16x16x32_bf16 v[128:131], v[152:155], v[184:187], v[128:131]
	v_mfma_f32_16x16x32_bf16 v[124:127], v[160:163], v[184:187], v[124:127]
	v_mfma_f32_16x16x32_bf16 v[120:123], v[152:155], v[192:195], v[120:123]
	v_mfma_f32_16x16x32_bf16 v[112:115], v[160:163], v[192:195], v[112:115]
	v_mfma_f32_16x16x32_bf16 v[104:107], v[152:155], v[224:227], v[104:107]
	v_mfma_f32_16x16x32_bf16 v[96:99], v[160:163], v[224:227], v[96:99]
	v_mfma_f32_16x16x32_bf16 v[88:91], v[152:155], v[238:241], v[88:91]
	v_mfma_f32_16x16x32_bf16 v[80:83], v[160:163], v[238:241], v[80:83]
	v_mfma_f32_16x16x32_bf16 v[128:131], v[156:159], v[188:191], v[128:131]
	v_mfma_f32_16x16x32_bf16 v[124:127], v[164:167], v[188:191], v[124:127]
	v_mfma_f32_16x16x32_bf16 v[120:123], v[156:159], v[196:199], v[120:123]
	v_mfma_f32_16x16x32_bf16 v[112:115], v[164:167], v[196:199], v[112:115]
	v_mfma_f32_16x16x32_bf16 v[104:107], v[156:159], v[228:231], v[104:107]
	v_mfma_f32_16x16x32_bf16 v[96:99], v[164:167], v[228:231], v[96:99]
	v_mfma_f32_16x16x32_bf16 v[88:91], v[156:159], v[242:245], v[88:91]
	v_mfma_f32_16x16x32_bf16 v[80:83], v[164:167], v[242:245], v[80:83]
	v_mfma_f32_16x16x32_bf16 v[116:119], v[168:171], v[184:187], v[116:119]
	v_mfma_f32_16x16x32_bf16 v[108:111], v[176:179], v[184:187], v[108:111]
	v_mfma_f32_16x16x32_bf16 v[100:103], v[168:171], v[192:195], v[100:103]
	v_mfma_f32_16x16x32_bf16 v[92:95], v[176:179], v[192:195], v[92:95]
	v_mfma_f32_16x16x32_bf16 v[84:87], v[168:171], v[224:227], v[84:87]
	v_mfma_f32_16x16x32_bf16 v[76:79], v[176:179], v[224:227], v[76:79]
	v_mfma_f32_16x16x32_bf16 v[72:75], v[168:171], v[238:241], v[72:75]
	v_mfma_f32_16x16x32_bf16 v[68:71], v[176:179], v[238:241], v[68:71]
	v_mfma_f32_16x16x32_bf16 v[116:119], v[172:175], v[188:191], v[116:119]
	v_mfma_f32_16x16x32_bf16 v[108:111], v[180:183], v[188:191], v[108:111]
	v_mfma_f32_16x16x32_bf16 v[100:103], v[172:175], v[196:199], v[100:103]
	v_mfma_f32_16x16x32_bf16 v[92:95], v[180:183], v[196:199], v[92:95]
	v_mfma_f32_16x16x32_bf16 v[84:87], v[172:175], v[228:231], v[84:87]
	v_mfma_f32_16x16x32_bf16 v[76:79], v[180:183], v[228:231], v[76:79]
	v_mfma_f32_16x16x32_bf16 v[72:75], v[172:175], v[242:245], v[72:75]
	v_mfma_f32_16x16x32_bf16 v[68:71], v[180:183], v[242:245], v[68:71]
	s_barrier
	s_add_i32 s31, s31, s47
	v_lshl_add_u64 v[146:147], s[42:43], 0, v[34:35]
	s_mov_b32 m0, s31
	ds_read_b128 v[184:187], v150 offset:16384
	ds_read_b128 v[188:191], v150 offset:17408
	ds_read_b128 v[192:195], v150 offset:18432
	ds_read_b128 v[196:199], v150 offset:19456
	ds_read_b128 v[224:227], v150 offset:20480
	ds_read_b128 v[228:231], v150 offset:21504
	ds_read_b128 v[238:241], v150 offset:22528
	ds_read_b128 v[242:245], v150 offset:23552
	global_load_lds_dwordx4 v[146:147], off
	s_add_i32 m0, s31, 0x2000
	s_add_u32 s64, s42, 0x80000
	v_lshl_add_u64 v[212:213], s[42:43], 0, v[132:133]
	s_addc_u32 s65, s43, 0
	s_add_i32 s31, s68, s47
	global_load_lds_dwordx4 v[212:213], off
	v_lshl_add_u64 v[232:233], s[64:65], 0, v[34:35]
	s_mov_b32 m0, s31
	v_lshl_add_u64 v[246:247], s[4:5], 0, v[134:135]
	global_load_lds_dwordx4 v[232:233], off
	v_lshl_add_u64 v[232:233], s[64:65], 0, v[132:133]
	s_add_i32 m0, s31, 0x2000
	s_nop 0
	global_load_lds_dwordx4 v[232:233], off
	v_lshl_add_u64 v[232:233], s[4:5], 0, v[138:139]
	s_mov_b32 m0, s48
	s_nop 0
	global_load_lds_dwordx4 v[232:233], off
	s_mov_b32 m0, s49
	s_nop 0
	global_load_lds_dwordx4 v[246:247], off
	s_waitcnt vmcnt(8)
	s_waitcnt lgkmcnt(0)
	s_barrier
	s_waitcnt lgkmcnt(0)
	v_mfma_f32_16x16x32_bf16 v[64:67], v[152:155], v[184:187], v[64:67]
	v_mfma_f32_16x16x32_bf16 v[60:63], v[160:163], v[184:187], v[60:63]
	v_mfma_f32_16x16x32_bf16 v[52:55], v[152:155], v[192:195], v[52:55]
	v_mfma_f32_16x16x32_bf16 v[44:47], v[160:163], v[192:195], v[44:47]
	v_mfma_f32_16x16x32_bf16 v[36:39], v[152:155], v[224:227], v[36:39]
	v_mfma_f32_16x16x32_bf16 v[26:29], v[160:163], v[224:227], v[26:29]
	v_mfma_f32_16x16x32_bf16 v[18:21], v[152:155], v[238:241], v[18:21]
	v_mfma_f32_16x16x32_bf16 v[10:13], v[160:163], v[238:241], v[10:13]
	v_mfma_f32_16x16x32_bf16 v[64:67], v[156:159], v[188:191], v[64:67]
	v_mfma_f32_16x16x32_bf16 v[60:63], v[164:167], v[188:191], v[60:63]
	v_mfma_f32_16x16x32_bf16 v[52:55], v[156:159], v[196:199], v[52:55]
	v_mfma_f32_16x16x32_bf16 v[44:47], v[164:167], v[196:199], v[44:47]
	v_mfma_f32_16x16x32_bf16 v[36:39], v[156:159], v[228:231], v[36:39]
	v_mfma_f32_16x16x32_bf16 v[26:29], v[164:167], v[228:231], v[26:29]
	v_mfma_f32_16x16x32_bf16 v[18:21], v[156:159], v[242:245], v[18:21]
	v_mfma_f32_16x16x32_bf16 v[10:13], v[164:167], v[242:245], v[10:13]
	v_mfma_f32_16x16x32_bf16 v[56:59], v[168:171], v[184:187], v[56:59]
	v_mfma_f32_16x16x32_bf16 v[48:51], v[176:179], v[184:187], v[48:51]
	v_mfma_f32_16x16x32_bf16 v[40:43], v[168:171], v[192:195], v[40:43]
	v_mfma_f32_16x16x32_bf16 v[30:33], v[176:179], v[192:195], v[30:33]
	v_mfma_f32_16x16x32_bf16 v[22:25], v[168:171], v[224:227], v[22:25]
	v_mfma_f32_16x16x32_bf16 v[14:17], v[176:179], v[224:227], v[14:17]
	v_mfma_f32_16x16x32_bf16 v[6:9], v[168:171], v[238:241], v[6:9]
	v_mfma_f32_16x16x32_bf16 v[2:5], v[176:179], v[238:241], v[2:5]
	v_mfma_f32_16x16x32_bf16 v[56:59], v[172:175], v[188:191], v[56:59]
	v_mfma_f32_16x16x32_bf16 v[48:51], v[180:183], v[188:191], v[48:51]
	v_mfma_f32_16x16x32_bf16 v[40:43], v[172:175], v[196:199], v[40:43]
	v_mfma_f32_16x16x32_bf16 v[30:33], v[180:183], v[196:199], v[30:33]
	v_mfma_f32_16x16x32_bf16 v[22:25], v[172:175], v[228:231], v[22:25]
	v_mfma_f32_16x16x32_bf16 v[14:17], v[180:183], v[228:231], v[14:17]
	v_mfma_f32_16x16x32_bf16 v[6:9], v[172:175], v[242:245], v[6:9]
	v_mfma_f32_16x16x32_bf16 v[2:5], v[180:183], v[242:245], v[2:5]
	s_barrier
	s_add_i32 s31, 0, 0x18000
	v_add_u32_e32 v151, s31, v148
	s_add_i32 s64, 0, 0x1c000
	ds_read_b128 v[152:155], v151
	ds_read_b128 v[156:159], v151 offset:1024
	ds_read_b128 v[160:163], v151 offset:2048
	ds_read_b128 v[164:167], v151 offset:3072
	v_add_u32_e32 v151, s64, v148
	ds_read_b128 v[168:171], v151
	ds_read_b128 v[172:175], v151 offset:1024
	ds_read_b128 v[176:179], v151 offset:2048
	ds_read_b128 v[180:183], v151 offset:3072
	s_mov_b32 m0, s50
	v_lshl_add_u64 v[248:249], s[4:5], 0, v[140:141]
	ds_read_b128 v[184:187], v150 offset:32768
	ds_read_b128 v[188:191], v150 offset:33792
	ds_read_b128 v[192:195], v150 offset:34816
	ds_read_b128 v[196:199], v150 offset:35840
	ds_read_b128 v[224:227], v150 offset:36864
	ds_read_b128 v[228:231], v150 offset:37888
	ds_read_b128 v[238:241], v150 offset:38912
	ds_read_b128 v[242:245], v150 offset:39936
	global_load_lds_dwordx4 v[248:249], off
	v_lshl_add_u64 v[248:249], s[4:5], 0, v[136:137]
	s_mov_b32 m0, s51
	s_nop 0
	global_load_lds_dwordx4 v[248:249], off
	s_waitcnt vmcnt(8)
	s_waitcnt lgkmcnt(0)
	s_barrier
	s_waitcnt lgkmcnt(0)
	v_mfma_f32_16x16x32_bf16 v[128:131], v[152:155], v[184:187], v[128:131]
	v_mfma_f32_16x16x32_bf16 v[124:127], v[160:163], v[184:187], v[124:127]
	v_mfma_f32_16x16x32_bf16 v[120:123], v[152:155], v[192:195], v[120:123]
	v_mfma_f32_16x16x32_bf16 v[112:115], v[160:163], v[192:195], v[112:115]
	v_mfma_f32_16x16x32_bf16 v[104:107], v[152:155], v[224:227], v[104:107]
	v_mfma_f32_16x16x32_bf16 v[96:99], v[160:163], v[224:227], v[96:99]
	v_mfma_f32_16x16x32_bf16 v[88:91], v[152:155], v[238:241], v[88:91]
	v_mfma_f32_16x16x32_bf16 v[80:83], v[160:163], v[238:241], v[80:83]
	v_mfma_f32_16x16x32_bf16 v[128:131], v[156:159], v[188:191], v[128:131]
	v_mfma_f32_16x16x32_bf16 v[124:127], v[164:167], v[188:191], v[124:127]
	v_mfma_f32_16x16x32_bf16 v[120:123], v[156:159], v[196:199], v[120:123]
	v_mfma_f32_16x16x32_bf16 v[112:115], v[164:167], v[196:199], v[112:115]
	v_mfma_f32_16x16x32_bf16 v[104:107], v[156:159], v[228:231], v[104:107]
	v_mfma_f32_16x16x32_bf16 v[96:99], v[164:167], v[228:231], v[96:99]
	v_mfma_f32_16x16x32_bf16 v[88:91], v[156:159], v[242:245], v[88:91]
	v_mfma_f32_16x16x32_bf16 v[80:83], v[164:167], v[242:245], v[80:83]
	v_mfma_f32_16x16x32_bf16 v[116:119], v[168:171], v[184:187], v[116:119]
	v_mfma_f32_16x16x32_bf16 v[108:111], v[176:179], v[184:187], v[108:111]
	v_mfma_f32_16x16x32_bf16 v[100:103], v[168:171], v[192:195], v[100:103]
	v_mfma_f32_16x16x32_bf16 v[92:95], v[176:179], v[192:195], v[92:95]
	v_mfma_f32_16x16x32_bf16 v[84:87], v[168:171], v[224:227], v[84:87]
	v_mfma_f32_16x16x32_bf16 v[76:79], v[176:179], v[224:227], v[76:79]
	v_mfma_f32_16x16x32_bf16 v[72:75], v[168:171], v[238:241], v[72:75]
	v_mfma_f32_16x16x32_bf16 v[68:71], v[176:179], v[238:241], v[68:71]
	v_mfma_f32_16x16x32_bf16 v[116:119], v[172:175], v[188:191], v[116:119]
	v_mfma_f32_16x16x32_bf16 v[108:111], v[180:183], v[188:191], v[108:111]
	v_mfma_f32_16x16x32_bf16 v[100:103], v[172:175], v[196:199], v[100:103]
	v_mfma_f32_16x16x32_bf16 v[92:95], v[180:183], v[196:199], v[92:95]
	v_mfma_f32_16x16x32_bf16 v[84:87], v[172:175], v[228:231], v[84:87]
	v_mfma_f32_16x16x32_bf16 v[76:79], v[180:183], v[228:231], v[76:79]
	v_mfma_f32_16x16x32_bf16 v[72:75], v[172:175], v[242:245], v[72:75]
	v_mfma_f32_16x16x32_bf16 v[68:71], v[180:183], v[242:245], v[68:71]
	s_barrier
	s_add_i32 s4, s31, s47
	v_lshl_add_u64 v[146:147], v[146:147], 0, s[78:79]
	s_mov_b32 m0, s4
	ds_read_b128 v[184:187], v150 offset:49152
	ds_read_b128 v[188:191], v150 offset:50176
	ds_read_b128 v[192:195], v150 offset:51200
	ds_read_b128 v[196:199], v150 offset:52224
	ds_read_b128 v[224:227], v150 offset:53248
	ds_read_b128 v[228:231], v150 offset:54272
	ds_read_b128 v[238:241], v150 offset:55296
	ds_read_b128 v[242:245], v150 offset:56320
	global_load_lds_dwordx4 v[146:147], off
	s_add_i32 m0, s4, 0x2000
	s_add_u32 s4, s42, 0x80080
	v_lshl_add_u64 v[146:147], v[212:213], 0, s[78:79]
	s_addc_u32 s5, s43, 0
	s_add_i32 s31, s64, s47
	global_load_lds_dwordx4 v[146:147], off
	v_lshl_add_u64 v[146:147], s[4:5], 0, v[34:35]
	s_mov_b32 m0, s31
	s_nop 0
	global_load_lds_dwordx4 v[146:147], off
	v_lshl_add_u64 v[146:147], s[4:5], 0, v[132:133]
	s_add_i32 m0, s31, 0x2000
	s_nop 0
	global_load_lds_dwordx4 v[146:147], off
	v_lshl_add_u64 v[146:147], v[232:233], 0, s[78:79]
	s_mov_b32 m0, s52
	s_nop 0
	global_load_lds_dwordx4 v[146:147], off
	v_lshl_add_u64 v[146:147], v[246:247], 0, s[78:79]
	s_mov_b32 m0, s53
	s_nop 0
	global_load_lds_dwordx4 v[146:147], off
	s_waitcnt vmcnt(8)
	s_waitcnt lgkmcnt(0)
	s_barrier
	s_waitcnt lgkmcnt(0)
	v_mfma_f32_16x16x32_bf16 v[64:67], v[152:155], v[184:187], v[64:67]
	v_mfma_f32_16x16x32_bf16 v[60:63], v[160:163], v[184:187], v[60:63]
	v_mfma_f32_16x16x32_bf16 v[52:55], v[152:155], v[192:195], v[52:55]
	v_mfma_f32_16x16x32_bf16 v[44:47], v[160:163], v[192:195], v[44:47]
	v_mfma_f32_16x16x32_bf16 v[36:39], v[152:155], v[224:227], v[36:39]
	v_mfma_f32_16x16x32_bf16 v[26:29], v[160:163], v[224:227], v[26:29]
	v_mfma_f32_16x16x32_bf16 v[18:21], v[152:155], v[238:241], v[18:21]
	v_mfma_f32_16x16x32_bf16 v[10:13], v[160:163], v[238:241], v[10:13]
	v_mfma_f32_16x16x32_bf16 v[64:67], v[156:159], v[188:191], v[64:67]
	v_mfma_f32_16x16x32_bf16 v[60:63], v[164:167], v[188:191], v[60:63]
	v_mfma_f32_16x16x32_bf16 v[52:55], v[156:159], v[196:199], v[52:55]
	v_mfma_f32_16x16x32_bf16 v[44:47], v[164:167], v[196:199], v[44:47]
	v_mfma_f32_16x16x32_bf16 v[36:39], v[156:159], v[228:231], v[36:39]
	v_mfma_f32_16x16x32_bf16 v[26:29], v[164:167], v[228:231], v[26:29]
	v_mfma_f32_16x16x32_bf16 v[18:21], v[156:159], v[242:245], v[18:21]
	v_mfma_f32_16x16x32_bf16 v[10:13], v[164:167], v[242:245], v[10:13]
	v_mfma_f32_16x16x32_bf16 v[56:59], v[168:171], v[184:187], v[56:59]
	v_mfma_f32_16x16x32_bf16 v[48:51], v[176:179], v[184:187], v[48:51]
	v_mfma_f32_16x16x32_bf16 v[40:43], v[168:171], v[192:195], v[40:43]
	v_mfma_f32_16x16x32_bf16 v[30:33], v[176:179], v[192:195], v[30:33]
	v_mfma_f32_16x16x32_bf16 v[22:25], v[168:171], v[224:227], v[22:25]
	v_mfma_f32_16x16x32_bf16 v[14:17], v[176:179], v[224:227], v[14:17]
	v_mfma_f32_16x16x32_bf16 v[6:9], v[168:171], v[238:241], v[6:9]
	v_mfma_f32_16x16x32_bf16 v[2:5], v[176:179], v[238:241], v[2:5]
	v_mfma_f32_16x16x32_bf16 v[56:59], v[172:175], v[188:191], v[56:59]
	v_mfma_f32_16x16x32_bf16 v[48:51], v[180:183], v[188:191], v[48:51]
	v_mfma_f32_16x16x32_bf16 v[40:43], v[172:175], v[196:199], v[40:43]
	v_mfma_f32_16x16x32_bf16 v[30:33], v[180:183], v[196:199], v[30:33]
	v_mfma_f32_16x16x32_bf16 v[22:25], v[172:175], v[228:231], v[22:25]
	v_mfma_f32_16x16x32_bf16 v[14:17], v[180:183], v[228:231], v[14:17]
	v_mfma_f32_16x16x32_bf16 v[6:9], v[172:175], v[242:245], v[6:9]
	v_mfma_f32_16x16x32_bf16 v[2:5], v[180:183], v[242:245], v[2:5]
	s_barrier
	s_add_i32 s29, s29, 2
	s_add_u32 s14, s14, 0x100
	s_addc_u32 s15, s15, 0
	s_add_u32 s38, s38, 0x100
	s_addc_u32 s39, s39, 0
	s_cmp_gt_u32 s29, 29
	s_cbranch_scc0 .LBB0_130
	s_setprio 0
	s_and_b64 vcc, exec, s[22:23]
	s_cbranch_vccz .LBB0_133
	s_barrier

.LBB0_606:
	s_add_u32 s23, s30, 0x100
	s_addc_u32 s25, s31, 0
	s_add_u32 s30, s34, 0x80
	v_mov_b32_e32 v2, 0
	s_addc_u32 s31, s35, 0
	s_mov_b32 s52, -2
	v_mov_b32_e32 v3, v2
	v_mov_b32_e32 v4, v2
	v_mov_b32_e32 v5, v2
	v_mov_b32_e32 v6, v2
	v_mov_b32_e32 v7, v2
	v_mov_b32_e32 v8, v2
	v_mov_b32_e32 v9, v2
	v_mov_b32_e32 v18, v2
	v_mov_b32_e32 v19, v2
	v_mov_b32_e32 v20, v2
	v_mov_b32_e32 v21, v2
	v_mov_b32_e32 v22, v2
	v_mov_b32_e32 v23, v2
	v_mov_b32_e32 v24, v2
	v_mov_b32_e32 v25, v2
	v_mov_b32_e32 v36, v2
	v_mov_b32_e32 v37, v2
	v_mov_b32_e32 v38, v2
	v_mov_b32_e32 v39, v2
	v_mov_b32_e32 v40, v2
	v_mov_b32_e32 v41, v2
	v_mov_b32_e32 v42, v2
	v_mov_b32_e32 v43, v2
	v_mov_b32_e32 v52, v2
	v_mov_b32_e32 v53, v2
	v_mov_b32_e32 v54, v2
	v_mov_b32_e32 v55, v2
	v_mov_b32_e32 v56, v2
	v_mov_b32_e32 v57, v2
	v_mov_b32_e32 v58, v2
	v_mov_b32_e32 v59, v2
	v_mov_b32_e32 v10, v2
	v_mov_b32_e32 v11, v2
	v_mov_b32_e32 v12, v2
	v_mov_b32_e32 v13, v2
	v_mov_b32_e32 v14, v2
	v_mov_b32_e32 v15, v2
	v_mov_b32_e32 v16, v2
	v_mov_b32_e32 v17, v2
	v_mov_b32_e32 v26, v2
	v_mov_b32_e32 v27, v2
	v_mov_b32_e32 v28, v2
	v_mov_b32_e32 v29, v2
	v_mov_b32_e32 v30, v2
	v_mov_b32_e32 v31, v2
	v_mov_b32_e32 v32, v2
	v_mov_b32_e32 v33, v2
	v_mov_b32_e32 v44, v2
	v_mov_b32_e32 v45, v2
	v_mov_b32_e32 v46, v2
	v_mov_b32_e32 v47, v2
	v_mov_b32_e32 v48, v2
	v_mov_b32_e32 v49, v2
	v_mov_b32_e32 v50, v2
	v_mov_b32_e32 v51, v2
	v_mov_b32_e32 v60, v2
	v_mov_b32_e32 v61, v2
	v_mov_b32_e32 v62, v2
	v_mov_b32_e32 v63, v2
	v_mov_b32_e32 v64, v2
	v_mov_b32_e32 v65, v2
	v_mov_b32_e32 v66, v2
	v_mov_b32_e32 v67, v2
	v_mov_b32_e32 v68, v2
	v_mov_b32_e32 v69, v2
	v_mov_b32_e32 v70, v2
	v_mov_b32_e32 v71, v2
	v_mov_b32_e32 v72, v2
	v_mov_b32_e32 v73, v2
	v_mov_b32_e32 v74, v2
	v_mov_b32_e32 v75, v2
	v_mov_b32_e32 v84, v2
	v_mov_b32_e32 v85, v2
	v_mov_b32_e32 v86, v2
	v_mov_b32_e32 v87, v2
	v_mov_b32_e32 v88, v2
	v_mov_b32_e32 v89, v2
	v_mov_b32_e32 v90, v2
	v_mov_b32_e32 v91, v2
	v_mov_b32_e32 v100, v2
	v_mov_b32_e32 v101, v2
	v_mov_b32_e32 v102, v2
	v_mov_b32_e32 v103, v2
	v_mov_b32_e32 v104, v2
	v_mov_b32_e32 v105, v2
	v_mov_b32_e32 v106, v2
	v_mov_b32_e32 v107, v2
	v_mov_b32_e32 v116, v2
	v_mov_b32_e32 v117, v2
	v_mov_b32_e32 v118, v2
	v_mov_b32_e32 v119, v2
	v_mov_b32_e32 v120, v2
	v_mov_b32_e32 v121, v2
	v_mov_b32_e32 v122, v2
	v_mov_b32_e32 v123, v2
	v_mov_b32_e32 v76, v2
	v_mov_b32_e32 v77, v2
	v_mov_b32_e32 v78, v2
	v_mov_b32_e32 v79, v2
	v_mov_b32_e32 v80, v2
	v_mov_b32_e32 v81, v2
	v_mov_b32_e32 v82, v2
	v_mov_b32_e32 v83, v2
	v_mov_b32_e32 v92, v2
	v_mov_b32_e32 v93, v2
	v_mov_b32_e32 v94, v2
	v_mov_b32_e32 v95, v2
	v_mov_b32_e32 v96, v2
	v_mov_b32_e32 v97, v2
	v_mov_b32_e32 v98, v2
	v_mov_b32_e32 v99, v2
	v_mov_b32_e32 v108, v2
	v_mov_b32_e32 v109, v2
	v_mov_b32_e32 v110, v2
	v_mov_b32_e32 v111, v2
	v_mov_b32_e32 v112, v2
	v_mov_b32_e32 v113, v2
	v_mov_b32_e32 v114, v2
	v_mov_b32_e32 v115, v2
	v_mov_b32_e32 v124, v2
	v_mov_b32_e32 v125, v2
	v_mov_b32_e32 v126, v2
	v_mov_b32_e32 v127, v2
	v_mov_b32_e32 v128, v2
	v_mov_b32_e32 v129, v2
	v_mov_b32_e32 v130, v2
	v_mov_b32_e32 v131, v2
	v_readfirstlane_b32 s96, v0
	s_nop 3
	s_bitcmp1_b32 s96, 8
	s_cbranch_scc0 .Lsp607
	s_setprio 1
.Lsp607:
.LBB0_607:
	s_add_u32 s4, s30, 0x80
	s_addc_u32 s5, s31, 0
	s_add_i32 s53, 0, 0x10000
	s_cmp_eq_u32 s52, 28
	s_cselect_b32 s5, s27, s5
	s_cselect_b32 s4, s26, s4
	v_add_u32_e32 v153, s53, v150
	s_cselect_b32 s35, s29, s25
	s_cselect_b32 s34, s28, s23
	s_add_i32 s56, 0, 0x14000
	ds_read_b128 v[146:149], v153
	ds_read_b128 v[154:157], v153 offset:1024
	ds_read_b128 v[158:161], v153 offset:2048
	ds_read_b128 v[162:165], v153 offset:3072
	v_add_u32_e32 v153, s56, v150
	ds_read_b128 v[166:169], v153
	ds_read_b128 v[170:173], v153 offset:1024
	ds_read_b128 v[174:177], v153 offset:2048
	ds_read_b128 v[178:181], v153 offset:3072
	v_lshl_add_u64 v[198:199], s[30:31], 0, v[144:145]
	s_add_i32 m0, s42, 0xc000
	ds_read_b128 v[182:185], v152
	ds_read_b128 v[186:189], v152 offset:1024
	ds_read_b128 v[190:193], v152 offset:2048
	ds_read_b128 v[194:197], v152 offset:3072
	ds_read_b128 v[224:227], v152 offset:4096
	ds_read_b128 v[228:231], v152 offset:5120
	ds_read_b128 v[238:241], v152 offset:6144
	ds_read_b128 v[242:245], v152 offset:7168
	global_load_lds_dwordx4 v[198:199], off
	v_lshl_add_u64 v[198:199], s[30:31], 0, v[142:143]
	s_add_i32 m0, s42, 0xe000
	s_nop 0
	global_load_lds_dwordx4 v[198:199], off
	s_waitcnt vmcnt(8)
	s_waitcnt lgkmcnt(0)
	s_barrier
	s_waitcnt lgkmcnt(0)
	v_mfma_f32_16x16x32_bf16 v[128:131], v[146:149], v[182:185], v[128:131]
	v_mfma_f32_16x16x32_bf16 v[124:127], v[158:161], v[182:185], v[124:127]
	v_mfma_f32_16x16x32_bf16 v[112:115], v[146:149], v[190:193], v[112:115]
	v_mfma_f32_16x16x32_bf16 v[108:111], v[158:161], v[190:193], v[108:111]
	v_mfma_f32_16x16x32_bf16 v[96:99], v[146:149], v[224:227], v[96:99]
	v_mfma_f32_16x16x32_bf16 v[92:95], v[158:161], v[224:227], v[92:95]
	v_mfma_f32_16x16x32_bf16 v[80:83], v[146:149], v[238:241], v[80:83]
	v_mfma_f32_16x16x32_bf16 v[76:79], v[158:161], v[238:241], v[76:79]
	v_mfma_f32_16x16x32_bf16 v[128:131], v[154:157], v[186:189], v[128:131]
	v_mfma_f32_16x16x32_bf16 v[124:127], v[162:165], v[186:189], v[124:127]
	v_mfma_f32_16x16x32_bf16 v[112:115], v[154:157], v[194:197], v[112:115]
	v_mfma_f32_16x16x32_bf16 v[108:111], v[162:165], v[194:197], v[108:111]
	v_mfma_f32_16x16x32_bf16 v[96:99], v[154:157], v[228:231], v[96:99]
	v_mfma_f32_16x16x32_bf16 v[92:95], v[162:165], v[228:231], v[92:95]
	v_mfma_f32_16x16x32_bf16 v[80:83], v[154:157], v[242:245], v[80:83]
	v_mfma_f32_16x16x32_bf16 v[76:79], v[162:165], v[242:245], v[76:79]
	v_mfma_f32_16x16x32_bf16 v[120:123], v[166:169], v[182:185], v[120:123]
	v_mfma_f32_16x16x32_bf16 v[116:119], v[174:177], v[182:185], v[116:119]
	v_mfma_f32_16x16x32_bf16 v[104:107], v[166:169], v[190:193], v[104:107]
	v_mfma_f32_16x16x32_bf16 v[100:103], v[174:177], v[190:193], v[100:103]
	v_mfma_f32_16x16x32_bf16 v[88:91], v[166:169], v[224:227], v[88:91]
	v_mfma_f32_16x16x32_bf16 v[84:87], v[174:177], v[224:227], v[84:87]
	v_mfma_f32_16x16x32_bf16 v[72:75], v[166:169], v[238:241], v[72:75]
	v_mfma_f32_16x16x32_bf16 v[68:71], v[174:177], v[238:241], v[68:71]
	v_mfma_f32_16x16x32_bf16 v[120:123], v[170:173], v[186:189], v[120:123]
	v_mfma_f32_16x16x32_bf16 v[116:119], v[178:181], v[186:189], v[116:119]
	v_mfma_f32_16x16x32_bf16 v[104:107], v[170:173], v[194:197], v[104:107]
	v_mfma_f32_16x16x32_bf16 v[100:103], v[178:181], v[194:197], v[100:103]
	v_mfma_f32_16x16x32_bf16 v[88:91], v[170:173], v[228:231], v[88:91]
	v_mfma_f32_16x16x32_bf16 v[84:87], v[178:181], v[228:231], v[84:87]
	v_mfma_f32_16x16x32_bf16 v[72:75], v[170:173], v[242:245], v[72:75]
	v_mfma_f32_16x16x32_bf16 v[68:71], v[178:181], v[242:245], v[68:71]
	s_barrier
	s_add_i32 s53, s53, s39
	v_lshl_add_u64 v[198:199], s[34:35], 0, v[34:35]
	s_mov_b32 m0, s53
	ds_read_b128 v[182:185], v152 offset:16384
	ds_read_b128 v[186:189], v152 offset:17408
	ds_read_b128 v[190:193], v152 offset:18432
	ds_read_b128 v[194:197], v152 offset:19456
	ds_read_b128 v[224:227], v152 offset:20480
	ds_read_b128 v[228:231], v152 offset:21504
	ds_read_b128 v[238:241], v152 offset:22528
	ds_read_b128 v[242:245], v152 offset:23552
	global_load_lds_dwordx4 v[198:199], off
	s_add_i32 m0, s53, 0x2000
	s_add_u32 s54, s34, 0x80000
	v_lshl_add_u64 v[212:213], s[34:35], 0, v[132:133]
	s_addc_u32 s55, s35, 0
	s_add_i32 s53, s56, s39
	global_load_lds_dwordx4 v[212:213], off
	v_lshl_add_u64 v[232:233], s[54:55], 0, v[34:35]
	s_mov_b32 m0, s53
	v_lshl_add_u64 v[246:247], s[4:5], 0, v[134:135]
	global_load_lds_dwordx4 v[232:233], off
	v_lshl_add_u64 v[232:233], s[54:55], 0, v[132:133]
	s_add_i32 m0, s53, 0x2000
	s_nop 0
	global_load_lds_dwordx4 v[232:233], off
	v_lshl_add_u64 v[232:233], s[4:5], 0, v[138:139]
	s_mov_b32 m0, s42
	s_nop 0
	global_load_lds_dwordx4 v[232:233], off
	s_mov_b32 m0, s43
	s_nop 0
	global_load_lds_dwordx4 v[246:247], off
	s_waitcnt vmcnt(8)
	s_waitcnt lgkmcnt(0)
	s_barrier
	s_waitcnt lgkmcnt(0)
	v_mfma_f32_16x16x32_bf16 v[64:67], v[146:149], v[182:185], v[64:67]
	v_mfma_f32_16x16x32_bf16 v[60:63], v[158:161], v[182:185], v[60:63]
	v_mfma_f32_16x16x32_bf16 v[48:51], v[146:149], v[190:193], v[48:51]
	v_mfma_f32_16x16x32_bf16 v[44:47], v[158:161], v[190:193], v[44:47]
	v_mfma_f32_16x16x32_bf16 v[30:33], v[146:149], v[224:227], v[30:33]
	v_mfma_f32_16x16x32_bf16 v[26:29], v[158:161], v[224:227], v[26:29]
	v_mfma_f32_16x16x32_bf16 v[14:17], v[146:149], v[238:241], v[14:17]
	v_mfma_f32_16x16x32_bf16 v[10:13], v[158:161], v[238:241], v[10:13]
	v_mfma_f32_16x16x32_bf16 v[64:67], v[154:157], v[186:189], v[64:67]
	v_mfma_f32_16x16x32_bf16 v[60:63], v[162:165], v[186:189], v[60:63]
	v_mfma_f32_16x16x32_bf16 v[48:51], v[154:157], v[194:197], v[48:51]
	v_mfma_f32_16x16x32_bf16 v[44:47], v[162:165], v[194:197], v[44:47]
	v_mfma_f32_16x16x32_bf16 v[30:33], v[154:157], v[228:231], v[30:33]
	v_mfma_f32_16x16x32_bf16 v[26:29], v[162:165], v[228:231], v[26:29]
	v_mfma_f32_16x16x32_bf16 v[14:17], v[154:157], v[242:245], v[14:17]
	v_mfma_f32_16x16x32_bf16 v[10:13], v[162:165], v[242:245], v[10:13]
	v_mfma_f32_16x16x32_bf16 v[56:59], v[166:169], v[182:185], v[56:59]
	v_mfma_f32_16x16x32_bf16 v[52:55], v[174:177], v[182:185], v[52:55]
	v_mfma_f32_16x16x32_bf16 v[40:43], v[166:169], v[190:193], v[40:43]
	v_mfma_f32_16x16x32_bf16 v[36:39], v[174:177], v[190:193], v[36:39]
	v_mfma_f32_16x16x32_bf16 v[22:25], v[166:169], v[224:227], v[22:25]
	v_mfma_f32_16x16x32_bf16 v[18:21], v[174:177], v[224:227], v[18:21]
	v_mfma_f32_16x16x32_bf16 v[6:9], v[166:169], v[238:241], v[6:9]
	v_mfma_f32_16x16x32_bf16 v[2:5], v[174:177], v[238:241], v[2:5]
	v_mfma_f32_16x16x32_bf16 v[56:59], v[170:173], v[186:189], v[56:59]
	v_mfma_f32_16x16x32_bf16 v[52:55], v[178:181], v[186:189], v[52:55]
	v_mfma_f32_16x16x32_bf16 v[40:43], v[170:173], v[194:197], v[40:43]
	v_mfma_f32_16x16x32_bf16 v[36:39], v[178:181], v[194:197], v[36:39]
	v_mfma_f32_16x16x32_bf16 v[22:25], v[170:173], v[228:231], v[22:25]
	v_mfma_f32_16x16x32_bf16 v[18:21], v[178:181], v[228:231], v[18:21]
	v_mfma_f32_16x16x32_bf16 v[6:9], v[170:173], v[242:245], v[6:9]
	v_mfma_f32_16x16x32_bf16 v[2:5], v[178:181], v[242:245], v[2:5]
	s_barrier
	s_add_i32 s53, 0, 0x18000
	v_add_u32_e32 v153, s53, v150
	s_add_i32 s54, 0, 0x1c000
	ds_read_b128 v[146:149], v153
	ds_read_b128 v[154:157], v153 offset:1024
	ds_read_b128 v[158:161], v153 offset:2048
	ds_read_b128 v[162:165], v153 offset:3072
	v_add_u32_e32 v153, s54, v150
	ds_read_b128 v[166:169], v153
	ds_read_b128 v[170:173], v153 offset:1024
	ds_read_b128 v[174:177], v153 offset:2048
	ds_read_b128 v[178:181], v153 offset:3072
	s_mov_b32 m0, s44
	v_lshl_add_u64 v[248:249], s[4:5], 0, v[140:141]
	ds_read_b128 v[182:185], v152 offset:32768
	ds_read_b128 v[186:189], v152 offset:33792
	ds_read_b128 v[190:193], v152 offset:34816
	ds_read_b128 v[194:197], v152 offset:35840
	ds_read_b128 v[224:227], v152 offset:36864
	ds_read_b128 v[228:231], v152 offset:37888
	ds_read_b128 v[238:241], v152 offset:38912
	ds_read_b128 v[242:245], v152 offset:39936
	global_load_lds_dwordx4 v[248:249], off
	v_lshl_add_u64 v[248:249], s[4:5], 0, v[136:137]
	s_mov_b32 m0, s45
	s_nop 0
	global_load_lds_dwordx4 v[248:249], off
	s_waitcnt vmcnt(8)
	s_waitcnt lgkmcnt(0)
	s_barrier
	s_waitcnt lgkmcnt(0)
	v_mfma_f32_16x16x32_bf16 v[128:131], v[146:149], v[182:185], v[128:131]
	v_mfma_f32_16x16x32_bf16 v[124:127], v[158:161], v[182:185], v[124:127]
	v_mfma_f32_16x16x32_bf16 v[112:115], v[146:149], v[190:193], v[112:115]
	v_mfma_f32_16x16x32_bf16 v[108:111], v[158:161], v[190:193], v[108:111]
	v_mfma_f32_16x16x32_bf16 v[96:99], v[146:149], v[224:227], v[96:99]
	v_mfma_f32_16x16x32_bf16 v[92:95], v[158:161], v[224:227], v[92:95]
	v_mfma_f32_16x16x32_bf16 v[80:83], v[146:149], v[238:241], v[80:83]
	v_mfma_f32_16x16x32_bf16 v[76:79], v[158:161], v[238:241], v[76:79]
	v_mfma_f32_16x16x32_bf16 v[128:131], v[154:157], v[186:189], v[128:131]
	v_mfma_f32_16x16x32_bf16 v[124:127], v[162:165], v[186:189], v[124:127]
	v_mfma_f32_16x16x32_bf16 v[112:115], v[154:157], v[194:197], v[112:115]
	v_mfma_f32_16x16x32_bf16 v[108:111], v[162:165], v[194:197], v[108:111]
	v_mfma_f32_16x16x32_bf16 v[96:99], v[154:157], v[228:231], v[96:99]
	v_mfma_f32_16x16x32_bf16 v[92:95], v[162:165], v[228:231], v[92:95]
	v_mfma_f32_16x16x32_bf16 v[80:83], v[154:157], v[242:245], v[80:83]
	v_mfma_f32_16x16x32_bf16 v[76:79], v[162:165], v[242:245], v[76:79]
	v_mfma_f32_16x16x32_bf16 v[120:123], v[166:169], v[182:185], v[120:123]
	v_mfma_f32_16x16x32_bf16 v[116:119], v[174:177], v[182:185], v[116:119]
	v_mfma_f32_16x16x32_bf16 v[104:107], v[166:169], v[190:193], v[104:107]
	v_mfma_f32_16x16x32_bf16 v[100:103], v[174:177], v[190:193], v[100:103]
	v_mfma_f32_16x16x32_bf16 v[88:91], v[166:169], v[224:227], v[88:91]
	v_mfma_f32_16x16x32_bf16 v[84:87], v[174:177], v[224:227], v[84:87]
	v_mfma_f32_16x16x32_bf16 v[72:75], v[166:169], v[238:241], v[72:75]
	v_mfma_f32_16x16x32_bf16 v[68:71], v[174:177], v[238:241], v[68:71]
	v_mfma_f32_16x16x32_bf16 v[120:123], v[170:173], v[186:189], v[120:123]
	v_mfma_f32_16x16x32_bf16 v[116:119], v[178:181], v[186:189], v[116:119]
	v_mfma_f32_16x16x32_bf16 v[104:107], v[170:173], v[194:197], v[104:107]
	v_mfma_f32_16x16x32_bf16 v[100:103], v[178:181], v[194:197], v[100:103]
	v_mfma_f32_16x16x32_bf16 v[88:91], v[170:173], v[228:231], v[88:91]
	v_mfma_f32_16x16x32_bf16 v[84:87], v[178:181], v[228:231], v[84:87]
	v_mfma_f32_16x16x32_bf16 v[72:75], v[170:173], v[242:245], v[72:75]
	v_mfma_f32_16x16x32_bf16 v[68:71], v[178:181], v[242:245], v[68:71]
	s_barrier
	s_add_i32 s4, s53, s39
	v_lshl_add_u64 v[198:199], v[198:199], 0, s[78:79]
	s_mov_b32 m0, s4
	ds_read_b128 v[182:185], v152 offset:49152
	ds_read_b128 v[186:189], v152 offset:50176
	ds_read_b128 v[190:193], v152 offset:51200
	ds_read_b128 v[194:197], v152 offset:52224
	ds_read_b128 v[224:227], v152 offset:53248
	ds_read_b128 v[228:231], v152 offset:54272
	ds_read_b128 v[238:241], v152 offset:55296
	ds_read_b128 v[242:245], v152 offset:56320
	global_load_lds_dwordx4 v[198:199], off
	s_add_i32 m0, s4, 0x2000
	s_add_u32 s4, s34, 0x80080
	v_lshl_add_u64 v[198:199], v[212:213], 0, s[78:79]
	s_addc_u32 s5, s35, 0
	s_add_i32 s34, s54, s39
	global_load_lds_dwordx4 v[198:199], off
	v_lshl_add_u64 v[198:199], s[4:5], 0, v[34:35]
	s_mov_b32 m0, s34
	s_nop 0
	global_load_lds_dwordx4 v[198:199], off
	v_lshl_add_u64 v[198:199], s[4:5], 0, v[132:133]
	s_add_i32 m0, s34, 0x2000
	s_nop 0
	global_load_lds_dwordx4 v[198:199], off
	v_lshl_add_u64 v[198:199], v[232:233], 0, s[78:79]
	s_mov_b32 m0, s46
	s_nop 0
	global_load_lds_dwordx4 v[198:199], off
	v_lshl_add_u64 v[198:199], v[246:247], 0, s[78:79]
	s_mov_b32 m0, s47
	s_nop 0
	global_load_lds_dwordx4 v[198:199], off
	s_waitcnt vmcnt(8)
	s_waitcnt lgkmcnt(0)
	s_barrier
	s_waitcnt lgkmcnt(0)
	v_mfma_f32_16x16x32_bf16 v[64:67], v[146:149], v[182:185], v[64:67]
	v_mfma_f32_16x16x32_bf16 v[60:63], v[158:161], v[182:185], v[60:63]
	v_mfma_f32_16x16x32_bf16 v[48:51], v[146:149], v[190:193], v[48:51]
	v_mfma_f32_16x16x32_bf16 v[44:47], v[158:161], v[190:193], v[44:47]
	v_mfma_f32_16x16x32_bf16 v[30:33], v[146:149], v[224:227], v[30:33]
	v_mfma_f32_16x16x32_bf16 v[26:29], v[158:161], v[224:227], v[26:29]
	v_mfma_f32_16x16x32_bf16 v[14:17], v[146:149], v[238:241], v[14:17]
	v_mfma_f32_16x16x32_bf16 v[10:13], v[158:161], v[238:241], v[10:13]
	v_mfma_f32_16x16x32_bf16 v[64:67], v[154:157], v[186:189], v[64:67]
	v_mfma_f32_16x16x32_bf16 v[60:63], v[162:165], v[186:189], v[60:63]
	v_mfma_f32_16x16x32_bf16 v[48:51], v[154:157], v[194:197], v[48:51]
	v_mfma_f32_16x16x32_bf16 v[44:47], v[162:165], v[194:197], v[44:47]
	v_mfma_f32_16x16x32_bf16 v[30:33], v[154:157], v[228:231], v[30:33]
	v_mfma_f32_16x16x32_bf16 v[26:29], v[162:165], v[228:231], v[26:29]
	v_mfma_f32_16x16x32_bf16 v[14:17], v[154:157], v[242:245], v[14:17]
	v_mfma_f32_16x16x32_bf16 v[10:13], v[162:165], v[242:245], v[10:13]
	v_mfma_f32_16x16x32_bf16 v[56:59], v[166:169], v[182:185], v[56:59]
	v_mfma_f32_16x16x32_bf16 v[52:55], v[174:177], v[182:185], v[52:55]
	v_mfma_f32_16x16x32_bf16 v[40:43], v[166:169], v[190:193], v[40:43]
	v_mfma_f32_16x16x32_bf16 v[36:39], v[174:177], v[190:193], v[36:39]
	v_mfma_f32_16x16x32_bf16 v[22:25], v[166:169], v[224:227], v[22:25]
	v_mfma_f32_16x16x32_bf16 v[18:21], v[174:177], v[224:227], v[18:21]
	v_mfma_f32_16x16x32_bf16 v[6:9], v[166:169], v[238:241], v[6:9]
	v_mfma_f32_16x16x32_bf16 v[2:5], v[174:177], v[238:241], v[2:5]
	v_mfma_f32_16x16x32_bf16 v[56:59], v[170:173], v[186:189], v[56:59]
	v_mfma_f32_16x16x32_bf16 v[52:55], v[178:181], v[186:189], v[52:55]
	v_mfma_f32_16x16x32_bf16 v[40:43], v[170:173], v[194:197], v[40:43]
	v_mfma_f32_16x16x32_bf16 v[36:39], v[178:181], v[194:197], v[36:39]
	v_mfma_f32_16x16x32_bf16 v[22:25], v[170:173], v[228:231], v[22:25]
	v_mfma_f32_16x16x32_bf16 v[18:21], v[178:181], v[228:231], v[18:21]
	v_mfma_f32_16x16x32_bf16 v[6:9], v[170:173], v[242:245], v[6:9]
	v_mfma_f32_16x16x32_bf16 v[2:5], v[178:181], v[242:245], v[2:5]
	s_barrier
	s_add_i32 s52, s52, 2
	s_add_u32 s23, s23, 0x100
	s_addc_u32 s25, s25, 0
	s_add_u32 s30, s30, 0x100
	s_addc_u32 s31, s31, 0
	s_cmp_gt_u32 s52, 29
	s_cbranch_scc0 .LBB0_607
	s_setprio 0
	s_and_b64 vcc, exec, s[20:21]
	s_cbranch_vccz .LBB0_610
	s_barrier

.LBB0_672:
	s_add_u32 s23, s34, 0x100
	s_addc_u32 s25, s35, 0
	s_add_u32 s30, s30, 0x80
	v_mov_b32_e32 v2, 0
	s_addc_u32 s31, s31, 0
	s_mov_b32 s57, -2
	v_mov_b32_e32 v3, v2
	v_mov_b32_e32 v4, v2
	v_mov_b32_e32 v5, v2
	v_mov_b32_e32 v6, v2
	v_mov_b32_e32 v7, v2
	v_mov_b32_e32 v8, v2
	v_mov_b32_e32 v9, v2
	v_mov_b32_e32 v18, v2
	v_mov_b32_e32 v19, v2
	v_mov_b32_e32 v20, v2
	v_mov_b32_e32 v21, v2
	v_mov_b32_e32 v22, v2
	v_mov_b32_e32 v23, v2
	v_mov_b32_e32 v24, v2
	v_mov_b32_e32 v25, v2
	v_mov_b32_e32 v36, v2
	v_mov_b32_e32 v37, v2
	v_mov_b32_e32 v38, v2
	v_mov_b32_e32 v39, v2
	v_mov_b32_e32 v40, v2
	v_mov_b32_e32 v41, v2
	v_mov_b32_e32 v42, v2
	v_mov_b32_e32 v43, v2
	v_mov_b32_e32 v52, v2
	v_mov_b32_e32 v53, v2
	v_mov_b32_e32 v54, v2
	v_mov_b32_e32 v55, v2
	v_mov_b32_e32 v56, v2
	v_mov_b32_e32 v57, v2
	v_mov_b32_e32 v58, v2
	v_mov_b32_e32 v59, v2
	v_mov_b32_e32 v10, v2
	v_mov_b32_e32 v11, v2
	v_mov_b32_e32 v12, v2
	v_mov_b32_e32 v13, v2
	v_mov_b32_e32 v14, v2
	v_mov_b32_e32 v15, v2
	v_mov_b32_e32 v16, v2
	v_mov_b32_e32 v17, v2
	v_mov_b32_e32 v26, v2
	v_mov_b32_e32 v27, v2
	v_mov_b32_e32 v28, v2
	v_mov_b32_e32 v29, v2
	v_mov_b32_e32 v30, v2
	v_mov_b32_e32 v31, v2
	v_mov_b32_e32 v32, v2
	v_mov_b32_e32 v33, v2
	v_mov_b32_e32 v44, v2
	v_mov_b32_e32 v45, v2
	v_mov_b32_e32 v46, v2
	v_mov_b32_e32 v47, v2
	v_mov_b32_e32 v48, v2
	v_mov_b32_e32 v49, v2
	v_mov_b32_e32 v50, v2
	v_mov_b32_e32 v51, v2
	v_mov_b32_e32 v60, v2
	v_mov_b32_e32 v61, v2
	v_mov_b32_e32 v62, v2
	v_mov_b32_e32 v63, v2
	v_mov_b32_e32 v64, v2
	v_mov_b32_e32 v65, v2
	v_mov_b32_e32 v66, v2
	v_mov_b32_e32 v67, v2
	v_mov_b32_e32 v68, v2
	v_mov_b32_e32 v69, v2
	v_mov_b32_e32 v70, v2
	v_mov_b32_e32 v71, v2
	v_mov_b32_e32 v72, v2
	v_mov_b32_e32 v73, v2
	v_mov_b32_e32 v74, v2
	v_mov_b32_e32 v75, v2
	v_mov_b32_e32 v84, v2
	v_mov_b32_e32 v85, v2
	v_mov_b32_e32 v86, v2
	v_mov_b32_e32 v87, v2
	v_mov_b32_e32 v88, v2
	v_mov_b32_e32 v89, v2
	v_mov_b32_e32 v90, v2
	v_mov_b32_e32 v91, v2
	v_mov_b32_e32 v100, v2
	v_mov_b32_e32 v101, v2
	v_mov_b32_e32 v102, v2
	v_mov_b32_e32 v103, v2
	v_mov_b32_e32 v104, v2
	v_mov_b32_e32 v105, v2
	v_mov_b32_e32 v106, v2
	v_mov_b32_e32 v107, v2
	v_mov_b32_e32 v116, v2
	v_mov_b32_e32 v117, v2
	v_mov_b32_e32 v118, v2
	v_mov_b32_e32 v119, v2
	v_mov_b32_e32 v120, v2
	v_mov_b32_e32 v121, v2
	v_mov_b32_e32 v122, v2
	v_mov_b32_e32 v123, v2
	v_mov_b32_e32 v76, v2
	v_mov_b32_e32 v77, v2
	v_mov_b32_e32 v78, v2
	v_mov_b32_e32 v79, v2
	v_mov_b32_e32 v80, v2
	v_mov_b32_e32 v81, v2
	v_mov_b32_e32 v82, v2
	v_mov_b32_e32 v83, v2
	v_mov_b32_e32 v92, v2
	v_mov_b32_e32 v93, v2
	v_mov_b32_e32 v94, v2
	v_mov_b32_e32 v95, v2
	v_mov_b32_e32 v96, v2
	v_mov_b32_e32 v97, v2
	v_mov_b32_e32 v98, v2
	v_mov_b32_e32 v99, v2
	v_mov_b32_e32 v108, v2
	v_mov_b32_e32 v109, v2
	v_mov_b32_e32 v110, v2
	v_mov_b32_e32 v111, v2
	v_mov_b32_e32 v112, v2
	v_mov_b32_e32 v113, v2
	v_mov_b32_e32 v114, v2
	v_mov_b32_e32 v115, v2
	v_mov_b32_e32 v124, v2
	v_mov_b32_e32 v125, v2
	v_mov_b32_e32 v126, v2
	v_mov_b32_e32 v127, v2
	v_mov_b32_e32 v128, v2
	v_mov_b32_e32 v129, v2
	v_mov_b32_e32 v130, v2
	v_mov_b32_e32 v131, v2
	v_readfirstlane_b32 s96, v0
	s_nop 3
	s_bitcmp1_b32 s96, 8
	s_cbranch_scc0 .Lsp673
	s_setprio 1
.Lsp673:
.LBB0_673:
	s_add_u32 s4, s30, 0x80
	s_addc_u32 s5, s31, 0
	s_add_i32 s64, 0, 0x10000
	s_cmp_eq_u32 s57, 12
	s_cselect_b32 s5, s27, s5
	s_cselect_b32 s4, s26, s4
	s_cselect_b32 s35, s29, s25
	s_cselect_b32 s34, s28, s23
	s_add_i32 s68, 0, 0x14000
	v_add_u32_e32 v144, s64, v190
	v_add_u32_e32 v160, s68, v190
	ds_read_b128 v[132:135], v144
	ds_read_b128 v[136:139], v144 offset:1024
	ds_read_b128 v[140:143], v144 offset:2048
	ds_read_b128 v[144:147], v144 offset:3072
	ds_read_b128 v[148:151], v160
	ds_read_b128 v[152:155], v160 offset:1024
	ds_read_b128 v[156:159], v160 offset:2048
	ds_read_b128 v[160:163], v160 offset:3072
	v_lshl_add_u64 v[164:165], s[30:31], 0, v[178:179]
	s_add_i32 m0, s38, 0xc000
	ds_read_b128 v[180:183], v192
	ds_read_b128 v[184:187], v192 offset:1024
	ds_read_b128 v[194:197], v192 offset:2048
	ds_read_b128 v[224:227], v192 offset:3072
	ds_read_b128 v[228:231], v192 offset:4096
	ds_read_b128 v[238:241], v192 offset:5120
	ds_read_b128 v[242:245], v192 offset:6144
	ds_read_b128 v[246:249], v192 offset:7168
	global_load_lds_dwordx4 v[164:165], off
	v_lshl_add_u64 v[164:165], s[30:31], 0, v[176:177]
	s_add_i32 m0, s38, 0xe000
	s_nop 0
	global_load_lds_dwordx4 v[164:165], off
	s_waitcnt vmcnt(8)
	s_waitcnt lgkmcnt(0)
	s_barrier
	s_waitcnt lgkmcnt(0)
	v_mfma_f32_16x16x32_bf16 v[128:131], v[132:135], v[180:183], v[128:131]
	v_mfma_f32_16x16x32_bf16 v[124:127], v[140:143], v[180:183], v[124:127]
	v_mfma_f32_16x16x32_bf16 v[112:115], v[132:135], v[194:197], v[112:115]
	v_mfma_f32_16x16x32_bf16 v[108:111], v[140:143], v[194:197], v[108:111]
	v_mfma_f32_16x16x32_bf16 v[96:99], v[132:135], v[228:231], v[96:99]
	v_mfma_f32_16x16x32_bf16 v[92:95], v[140:143], v[228:231], v[92:95]
	v_mfma_f32_16x16x32_bf16 v[80:83], v[132:135], v[242:245], v[80:83]
	v_mfma_f32_16x16x32_bf16 v[76:79], v[140:143], v[242:245], v[76:79]
	v_mfma_f32_16x16x32_bf16 v[128:131], v[136:139], v[184:187], v[128:131]
	v_mfma_f32_16x16x32_bf16 v[124:127], v[144:147], v[184:187], v[124:127]
	v_mfma_f32_16x16x32_bf16 v[112:115], v[136:139], v[224:227], v[112:115]
	v_mfma_f32_16x16x32_bf16 v[108:111], v[144:147], v[224:227], v[108:111]
	v_mfma_f32_16x16x32_bf16 v[96:99], v[136:139], v[238:241], v[96:99]
	v_mfma_f32_16x16x32_bf16 v[92:95], v[144:147], v[238:241], v[92:95]
	v_mfma_f32_16x16x32_bf16 v[80:83], v[136:139], v[246:249], v[80:83]
	v_mfma_f32_16x16x32_bf16 v[76:79], v[144:147], v[246:249], v[76:79]
	v_mfma_f32_16x16x32_bf16 v[120:123], v[148:151], v[180:183], v[120:123]
	v_mfma_f32_16x16x32_bf16 v[116:119], v[156:159], v[180:183], v[116:119]
	v_mfma_f32_16x16x32_bf16 v[104:107], v[148:151], v[194:197], v[104:107]
	v_mfma_f32_16x16x32_bf16 v[100:103], v[156:159], v[194:197], v[100:103]
	v_mfma_f32_16x16x32_bf16 v[88:91], v[148:151], v[228:231], v[88:91]
	v_mfma_f32_16x16x32_bf16 v[84:87], v[156:159], v[228:231], v[84:87]
	v_mfma_f32_16x16x32_bf16 v[72:75], v[148:151], v[242:245], v[72:75]
	v_mfma_f32_16x16x32_bf16 v[68:71], v[156:159], v[242:245], v[68:71]
	v_mfma_f32_16x16x32_bf16 v[120:123], v[152:155], v[184:187], v[120:123]
	v_mfma_f32_16x16x32_bf16 v[116:119], v[160:163], v[184:187], v[116:119]
	v_mfma_f32_16x16x32_bf16 v[104:107], v[152:155], v[224:227], v[104:107]
	v_mfma_f32_16x16x32_bf16 v[100:103], v[160:163], v[224:227], v[100:103]
	v_mfma_f32_16x16x32_bf16 v[88:91], v[152:155], v[238:241], v[88:91]
	v_mfma_f32_16x16x32_bf16 v[84:87], v[160:163], v[238:241], v[84:87]
	v_mfma_f32_16x16x32_bf16 v[72:75], v[152:155], v[246:249], v[72:75]
	v_mfma_f32_16x16x32_bf16 v[68:71], v[160:163], v[246:249], v[68:71]
	s_barrier
	s_add_i32 s64, s64, s37
	v_lshl_add_u64 v[164:165], s[34:35], 0, v[34:35]
	s_mov_b32 m0, s64
	ds_read_b128 v[180:183], v192 offset:16384
	ds_read_b128 v[184:187], v192 offset:17408
	ds_read_b128 v[194:197], v192 offset:18432
	ds_read_b128 v[224:227], v192 offset:19456
	ds_read_b128 v[228:231], v192 offset:20480
	ds_read_b128 v[238:241], v192 offset:21504
	ds_read_b128 v[242:245], v192 offset:22528
	ds_read_b128 v[246:249], v192 offset:23552
	global_load_lds_dwordx4 v[164:165], off
	s_add_i32 m0, s64, 0x2000
	s_add_u32 s64, s34, 0x40000
	v_lshl_add_u64 v[188:189], s[34:35], 0, v[174:175]
	s_addc_u32 s65, s35, 0
	s_add_i32 s68, s68, s37
	global_load_lds_dwordx4 v[188:189], off
	v_lshl_add_u64 v[198:199], s[64:65], 0, v[34:35]
	s_mov_b32 m0, s68
	v_lshl_add_u64 v[212:213], s[4:5], 0, v[170:171]
	global_load_lds_dwordx4 v[198:199], off
	v_lshl_add_u64 v[198:199], s[64:65], 0, v[174:175]
	s_add_i32 m0, s68, 0x2000
	s_nop 0
	global_load_lds_dwordx4 v[198:199], off
	v_lshl_add_u64 v[198:199], s[4:5], 0, v[166:167]
	s_mov_b32 m0, s38
	s_nop 0
	global_load_lds_dwordx4 v[198:199], off
	s_mov_b32 m0, s39
	s_nop 0
	global_load_lds_dwordx4 v[212:213], off
	s_waitcnt vmcnt(8)
	s_waitcnt lgkmcnt(0)
	s_barrier
	s_waitcnt lgkmcnt(0)
	v_mfma_f32_16x16x32_bf16 v[64:67], v[132:135], v[180:183], v[64:67]
	v_mfma_f32_16x16x32_bf16 v[60:63], v[140:143], v[180:183], v[60:63]
	v_mfma_f32_16x16x32_bf16 v[48:51], v[132:135], v[194:197], v[48:51]
	v_mfma_f32_16x16x32_bf16 v[44:47], v[140:143], v[194:197], v[44:47]
	v_mfma_f32_16x16x32_bf16 v[30:33], v[132:135], v[228:231], v[30:33]
	v_mfma_f32_16x16x32_bf16 v[26:29], v[140:143], v[228:231], v[26:29]
	v_mfma_f32_16x16x32_bf16 v[14:17], v[132:135], v[242:245], v[14:17]
	v_mfma_f32_16x16x32_bf16 v[10:13], v[140:143], v[242:245], v[10:13]
	v_mfma_f32_16x16x32_bf16 v[64:67], v[136:139], v[184:187], v[64:67]
	v_mfma_f32_16x16x32_bf16 v[60:63], v[144:147], v[184:187], v[60:63]
	v_mfma_f32_16x16x32_bf16 v[48:51], v[136:139], v[224:227], v[48:51]
	v_mfma_f32_16x16x32_bf16 v[44:47], v[144:147], v[224:227], v[44:47]
	v_mfma_f32_16x16x32_bf16 v[30:33], v[136:139], v[238:241], v[30:33]
	v_mfma_f32_16x16x32_bf16 v[26:29], v[144:147], v[238:241], v[26:29]
	v_mfma_f32_16x16x32_bf16 v[14:17], v[136:139], v[246:249], v[14:17]
	v_mfma_f32_16x16x32_bf16 v[10:13], v[144:147], v[246:249], v[10:13]
	v_mfma_f32_16x16x32_bf16 v[56:59], v[148:151], v[180:183], v[56:59]
	v_mfma_f32_16x16x32_bf16 v[52:55], v[156:159], v[180:183], v[52:55]
	v_mfma_f32_16x16x32_bf16 v[40:43], v[148:151], v[194:197], v[40:43]
	v_mfma_f32_16x16x32_bf16 v[36:39], v[156:159], v[194:197], v[36:39]
	v_mfma_f32_16x16x32_bf16 v[22:25], v[148:151], v[228:231], v[22:25]
	v_mfma_f32_16x16x32_bf16 v[18:21], v[156:159], v[228:231], v[18:21]
	v_mfma_f32_16x16x32_bf16 v[6:9], v[148:151], v[242:245], v[6:9]
	v_mfma_f32_16x16x32_bf16 v[2:5], v[156:159], v[242:245], v[2:5]
	v_mfma_f32_16x16x32_bf16 v[56:59], v[152:155], v[184:187], v[56:59]
	v_mfma_f32_16x16x32_bf16 v[52:55], v[160:163], v[184:187], v[52:55]
	v_mfma_f32_16x16x32_bf16 v[40:43], v[152:155], v[224:227], v[40:43]
	v_mfma_f32_16x16x32_bf16 v[36:39], v[160:163], v[224:227], v[36:39]
	v_mfma_f32_16x16x32_bf16 v[22:25], v[152:155], v[238:241], v[22:25]
	v_mfma_f32_16x16x32_bf16 v[18:21], v[160:163], v[238:241], v[18:21]
	v_mfma_f32_16x16x32_bf16 v[6:9], v[152:155], v[246:249], v[6:9]
	v_mfma_f32_16x16x32_bf16 v[2:5], v[160:163], v[246:249], v[2:5]
	s_barrier
	s_add_i32 s64, 0, 0x18000
	s_add_i32 s65, 0, 0x1c000
	v_add_u32_e32 v144, s64, v190
	v_add_u32_e32 v160, s65, v190
	ds_read_b128 v[132:135], v144
	ds_read_b128 v[136:139], v144 offset:1024
	ds_read_b128 v[140:143], v144 offset:2048
	ds_read_b128 v[144:147], v144 offset:3072
	ds_read_b128 v[148:151], v160
	ds_read_b128 v[152:155], v160 offset:1024
	ds_read_b128 v[156:159], v160 offset:2048
	ds_read_b128 v[160:163], v160 offset:3072
	s_mov_b32 m0, s46
	v_lshl_add_u64 v[232:233], s[4:5], 0, v[168:169]
	ds_read_b128 v[180:183], v192 offset:32768
	ds_read_b128 v[184:187], v192 offset:33792
	ds_read_b128 v[194:197], v192 offset:34816
	ds_read_b128 v[224:227], v192 offset:35840
	ds_read_b128 v[228:231], v192 offset:36864
	ds_read_b128 v[238:241], v192 offset:37888
	ds_read_b128 v[242:245], v192 offset:38912
	ds_read_b128 v[246:249], v192 offset:39936
	global_load_lds_dwordx4 v[232:233], off
	v_lshl_add_u64 v[232:233], s[4:5], 0, v[172:173]
	s_mov_b32 m0, s47
	s_nop 0
	global_load_lds_dwordx4 v[232:233], off
	s_waitcnt vmcnt(8)
	s_waitcnt lgkmcnt(0)
	s_barrier
	s_waitcnt lgkmcnt(0)
	v_mfma_f32_16x16x32_bf16 v[128:131], v[132:135], v[180:183], v[128:131]
	v_mfma_f32_16x16x32_bf16 v[124:127], v[140:143], v[180:183], v[124:127]
	v_mfma_f32_16x16x32_bf16 v[112:115], v[132:135], v[194:197], v[112:115]
	v_mfma_f32_16x16x32_bf16 v[108:111], v[140:143], v[194:197], v[108:111]
	v_mfma_f32_16x16x32_bf16 v[96:99], v[132:135], v[228:231], v[96:99]
	v_mfma_f32_16x16x32_bf16 v[92:95], v[140:143], v[228:231], v[92:95]
	v_mfma_f32_16x16x32_bf16 v[80:83], v[132:135], v[242:245], v[80:83]
	v_mfma_f32_16x16x32_bf16 v[76:79], v[140:143], v[242:245], v[76:79]
	v_mfma_f32_16x16x32_bf16 v[128:131], v[136:139], v[184:187], v[128:131]
	v_mfma_f32_16x16x32_bf16 v[124:127], v[144:147], v[184:187], v[124:127]
	v_mfma_f32_16x16x32_bf16 v[112:115], v[136:139], v[224:227], v[112:115]
	v_mfma_f32_16x16x32_bf16 v[108:111], v[144:147], v[224:227], v[108:111]
	v_mfma_f32_16x16x32_bf16 v[96:99], v[136:139], v[238:241], v[96:99]
	v_mfma_f32_16x16x32_bf16 v[92:95], v[144:147], v[238:241], v[92:95]
	v_mfma_f32_16x16x32_bf16 v[80:83], v[136:139], v[246:249], v[80:83]
	v_mfma_f32_16x16x32_bf16 v[76:79], v[144:147], v[246:249], v[76:79]
	v_mfma_f32_16x16x32_bf16 v[120:123], v[148:151], v[180:183], v[120:123]
	v_mfma_f32_16x16x32_bf16 v[116:119], v[156:159], v[180:183], v[116:119]
	v_mfma_f32_16x16x32_bf16 v[104:107], v[148:151], v[194:197], v[104:107]
	v_mfma_f32_16x16x32_bf16 v[100:103], v[156:159], v[194:197], v[100:103]
	v_mfma_f32_16x16x32_bf16 v[88:91], v[148:151], v[228:231], v[88:91]
	v_mfma_f32_16x16x32_bf16 v[84:87], v[156:159], v[228:231], v[84:87]
	v_mfma_f32_16x16x32_bf16 v[72:75], v[148:151], v[242:245], v[72:75]
	v_mfma_f32_16x16x32_bf16 v[68:71], v[156:159], v[242:245], v[68:71]
	v_mfma_f32_16x16x32_bf16 v[120:123], v[152:155], v[184:187], v[120:123]
	v_mfma_f32_16x16x32_bf16 v[116:119], v[160:163], v[184:187], v[116:119]
	v_mfma_f32_16x16x32_bf16 v[104:107], v[152:155], v[224:227], v[104:107]
	v_mfma_f32_16x16x32_bf16 v[100:103], v[160:163], v[224:227], v[100:103]
	v_mfma_f32_16x16x32_bf16 v[88:91], v[152:155], v[238:241], v[88:91]
	v_mfma_f32_16x16x32_bf16 v[84:87], v[160:163], v[238:241], v[84:87]
	v_mfma_f32_16x16x32_bf16 v[72:75], v[152:155], v[246:249], v[72:75]
	v_mfma_f32_16x16x32_bf16 v[68:71], v[160:163], v[246:249], v[68:71]
	s_barrier
	s_add_i32 s4, s64, s37
	v_lshl_add_u64 v[164:165], v[164:165], 0, s[78:79]
	s_mov_b32 m0, s4
	ds_read_b128 v[180:183], v192 offset:49152
	ds_read_b128 v[184:187], v192 offset:50176
	ds_read_b128 v[194:197], v192 offset:51200
	ds_read_b128 v[224:227], v192 offset:52224
	ds_read_b128 v[228:231], v192 offset:53248
	ds_read_b128 v[238:241], v192 offset:54272
	ds_read_b128 v[242:245], v192 offset:55296
	ds_read_b128 v[246:249], v192 offset:56320
	global_load_lds_dwordx4 v[164:165], off
	s_add_i32 m0, s4, 0x2000
	s_add_u32 s4, s34, 0x40080
	v_lshl_add_u64 v[164:165], v[188:189], 0, s[78:79]
	s_addc_u32 s5, s35, 0
	s_add_i32 s34, s65, s37
	global_load_lds_dwordx4 v[164:165], off
	v_lshl_add_u64 v[164:165], s[4:5], 0, v[34:35]
	s_mov_b32 m0, s34
	s_nop 0
	global_load_lds_dwordx4 v[164:165], off
	v_lshl_add_u64 v[164:165], s[4:5], 0, v[174:175]
	s_add_i32 m0, s34, 0x2000
	s_nop 0
	global_load_lds_dwordx4 v[164:165], off
	v_lshl_add_u64 v[164:165], v[198:199], 0, s[78:79]
	s_mov_b32 m0, s52
	s_nop 0
	global_load_lds_dwordx4 v[164:165], off
	v_lshl_add_u64 v[164:165], v[212:213], 0, s[78:79]
	s_mov_b32 m0, s53
	s_nop 0
	global_load_lds_dwordx4 v[164:165], off
	s_waitcnt vmcnt(8)
	s_waitcnt lgkmcnt(0)
	s_barrier
	s_waitcnt lgkmcnt(0)
	v_mfma_f32_16x16x32_bf16 v[64:67], v[132:135], v[180:183], v[64:67]
	v_mfma_f32_16x16x32_bf16 v[60:63], v[140:143], v[180:183], v[60:63]
	v_mfma_f32_16x16x32_bf16 v[48:51], v[132:135], v[194:197], v[48:51]
	v_mfma_f32_16x16x32_bf16 v[44:47], v[140:143], v[194:197], v[44:47]
	v_mfma_f32_16x16x32_bf16 v[30:33], v[132:135], v[228:231], v[30:33]
	v_mfma_f32_16x16x32_bf16 v[26:29], v[140:143], v[228:231], v[26:29]
	v_mfma_f32_16x16x32_bf16 v[14:17], v[132:135], v[242:245], v[14:17]
	v_mfma_f32_16x16x32_bf16 v[10:13], v[140:143], v[242:245], v[10:13]
	v_mfma_f32_16x16x32_bf16 v[64:67], v[136:139], v[184:187], v[64:67]
	v_mfma_f32_16x16x32_bf16 v[60:63], v[144:147], v[184:187], v[60:63]
	v_mfma_f32_16x16x32_bf16 v[48:51], v[136:139], v[224:227], v[48:51]
	v_mfma_f32_16x16x32_bf16 v[44:47], v[144:147], v[224:227], v[44:47]
	v_mfma_f32_16x16x32_bf16 v[30:33], v[136:139], v[238:241], v[30:33]
	v_mfma_f32_16x16x32_bf16 v[26:29], v[144:147], v[238:241], v[26:29]
	v_mfma_f32_16x16x32_bf16 v[14:17], v[136:139], v[246:249], v[14:17]
	v_mfma_f32_16x16x32_bf16 v[10:13], v[144:147], v[246:249], v[10:13]
	v_mfma_f32_16x16x32_bf16 v[56:59], v[148:151], v[180:183], v[56:59]
	v_mfma_f32_16x16x32_bf16 v[52:55], v[156:159], v[180:183], v[52:55]
	v_mfma_f32_16x16x32_bf16 v[40:43], v[148:151], v[194:197], v[40:43]
	v_mfma_f32_16x16x32_bf16 v[36:39], v[156:159], v[194:197], v[36:39]
	v_mfma_f32_16x16x32_bf16 v[22:25], v[148:151], v[228:231], v[22:25]
	v_mfma_f32_16x16x32_bf16 v[18:21], v[156:159], v[228:231], v[18:21]
	v_mfma_f32_16x16x32_bf16 v[6:9], v[148:151], v[242:245], v[6:9]
	v_mfma_f32_16x16x32_bf16 v[2:5], v[156:159], v[242:245], v[2:5]
	v_mfma_f32_16x16x32_bf16 v[56:59], v[152:155], v[184:187], v[56:59]
	v_mfma_f32_16x16x32_bf16 v[52:55], v[160:163], v[184:187], v[52:55]
	v_mfma_f32_16x16x32_bf16 v[40:43], v[152:155], v[224:227], v[40:43]
	v_mfma_f32_16x16x32_bf16 v[36:39], v[160:163], v[224:227], v[36:39]
	v_mfma_f32_16x16x32_bf16 v[22:25], v[152:155], v[238:241], v[22:25]
	v_mfma_f32_16x16x32_bf16 v[18:21], v[160:163], v[238:241], v[18:21]
	v_mfma_f32_16x16x32_bf16 v[6:9], v[152:155], v[246:249], v[6:9]
	v_mfma_f32_16x16x32_bf16 v[2:5], v[160:163], v[246:249], v[2:5]
	s_barrier
	s_add_i32 s57, s57, 2
	s_add_u32 s23, s23, 0x100
	s_addc_u32 s25, s25, 0
	s_add_u32 s30, s30, 0x100
	s_addc_u32 s31, s31, 0
	s_cmp_gt_u32 s57, 13
	s_cbranch_scc0 .LBB0_673
	s_setprio 0
	s_and_b64 vcc, exec, s[20:21]
	s_cbranch_vccz .LBB0_676
	s_barrier

.LBB0_786:
	s_add_u32 s29, s38, 0x100
	s_addc_u32 s31, s39, 0
	s_add_u32 s38, s44, 0x80
	v_mov_b32_e32 v2, 0
	s_addc_u32 s39, s45, 0
	s_mov_b32 s68, -2
	v_mov_b32_e32 v3, v2
	v_mov_b32_e32 v4, v2
	v_mov_b32_e32 v5, v2
	v_mov_b32_e32 v6, v2
	v_mov_b32_e32 v7, v2
	v_mov_b32_e32 v8, v2
	v_mov_b32_e32 v9, v2
	v_mov_b32_e32 v14, v2
	v_mov_b32_e32 v15, v2
	v_mov_b32_e32 v16, v2
	v_mov_b32_e32 v17, v2
	v_mov_b32_e32 v18, v2
	v_mov_b32_e32 v19, v2
	v_mov_b32_e32 v20, v2
	v_mov_b32_e32 v21, v2
	v_mov_b32_e32 v30, v2
	v_mov_b32_e32 v31, v2
	v_mov_b32_e32 v32, v2
	v_mov_b32_e32 v33, v2
	v_mov_b32_e32 v36, v2
	v_mov_b32_e32 v37, v2
	v_mov_b32_e32 v38, v2
	v_mov_b32_e32 v39, v2
	v_mov_b32_e32 v48, v2
	v_mov_b32_e32 v49, v2
	v_mov_b32_e32 v50, v2
	v_mov_b32_e32 v51, v2
	v_mov_b32_e32 v52, v2
	v_mov_b32_e32 v53, v2
	v_mov_b32_e32 v54, v2
	v_mov_b32_e32 v55, v2
	v_mov_b32_e32 v10, v2
	v_mov_b32_e32 v11, v2
	v_mov_b32_e32 v12, v2
	v_mov_b32_e32 v13, v2
	v_mov_b32_e32 v22, v2
	v_mov_b32_e32 v23, v2
	v_mov_b32_e32 v24, v2
	v_mov_b32_e32 v25, v2
	v_mov_b32_e32 v26, v2
	v_mov_b32_e32 v27, v2
	v_mov_b32_e32 v28, v2
	v_mov_b32_e32 v29, v2
	v_mov_b32_e32 v40, v2
	v_mov_b32_e32 v41, v2
	v_mov_b32_e32 v42, v2
	v_mov_b32_e32 v43, v2
	v_mov_b32_e32 v44, v2
	v_mov_b32_e32 v45, v2
	v_mov_b32_e32 v46, v2
	v_mov_b32_e32 v47, v2
	v_mov_b32_e32 v56, v2
	v_mov_b32_e32 v57, v2
	v_mov_b32_e32 v58, v2
	v_mov_b32_e32 v59, v2
	v_mov_b32_e32 v60, v2
	v_mov_b32_e32 v61, v2
	v_mov_b32_e32 v62, v2
	v_mov_b32_e32 v63, v2
	v_mov_b32_e32 v64, v2
	v_mov_b32_e32 v65, v2
	v_mov_b32_e32 v66, v2
	v_mov_b32_e32 v67, v2
	v_mov_b32_e32 v68, v2
	v_mov_b32_e32 v69, v2
	v_mov_b32_e32 v70, v2
	v_mov_b32_e32 v71, v2
	v_mov_b32_e32 v72, v2
	v_mov_b32_e32 v73, v2
	v_mov_b32_e32 v74, v2
	v_mov_b32_e32 v75, v2
	v_mov_b32_e32 v80, v2
	v_mov_b32_e32 v81, v2
	v_mov_b32_e32 v82, v2
	v_mov_b32_e32 v83, v2
	v_mov_b32_e32 v84, v2
	v_mov_b32_e32 v85, v2
	v_mov_b32_e32 v86, v2
	v_mov_b32_e32 v87, v2
	v_mov_b32_e32 v96, v2
	v_mov_b32_e32 v97, v2
	v_mov_b32_e32 v98, v2
	v_mov_b32_e32 v99, v2
	v_mov_b32_e32 v100, v2
	v_mov_b32_e32 v101, v2
	v_mov_b32_e32 v102, v2
	v_mov_b32_e32 v103, v2
	v_mov_b32_e32 v112, v2
	v_mov_b32_e32 v113, v2
	v_mov_b32_e32 v114, v2
	v_mov_b32_e32 v115, v2
	v_mov_b32_e32 v116, v2
	v_mov_b32_e32 v117, v2
	v_mov_b32_e32 v118, v2
	v_mov_b32_e32 v119, v2
	v_mov_b32_e32 v76, v2
	v_mov_b32_e32 v77, v2
	v_mov_b32_e32 v78, v2
	v_mov_b32_e32 v79, v2
	v_mov_b32_e32 v88, v2
	v_mov_b32_e32 v89, v2
	v_mov_b32_e32 v90, v2
	v_mov_b32_e32 v91, v2
	v_mov_b32_e32 v92, v2
	v_mov_b32_e32 v93, v2
	v_mov_b32_e32 v94, v2
	v_mov_b32_e32 v95, v2
	v_mov_b32_e32 v104, v2
	v_mov_b32_e32 v105, v2
	v_mov_b32_e32 v106, v2
	v_mov_b32_e32 v107, v2
	v_mov_b32_e32 v108, v2
	v_mov_b32_e32 v109, v2
	v_mov_b32_e32 v110, v2
	v_mov_b32_e32 v111, v2
	v_mov_b32_e32 v120, v2
	v_mov_b32_e32 v121, v2
	v_mov_b32_e32 v122, v2
	v_mov_b32_e32 v123, v2
	v_mov_b32_e32 v124, v2
	v_mov_b32_e32 v125, v2
	v_mov_b32_e32 v126, v2
	v_mov_b32_e32 v127, v2
	v_mov_b32_e32 v128, v2
	v_mov_b32_e32 v129, v2
	v_mov_b32_e32 v130, v2
	v_mov_b32_e32 v131, v2
	v_readfirstlane_b32 s96, v0
	s_nop 3
	s_bitcmp1_b32 s96, 8
	s_cbranch_scc0 .Lsp787
	s_setprio 1
.Lsp787:
.LBB0_787:
	s_add_u32 s4, s38, 0x80
	s_addc_u32 s5, s39, 0
	s_add_i32 s69, 0, 0x10000
	s_cmp_eq_u32 s68, 28
	s_cselect_b32 s5, s35, s5
	s_cselect_b32 s4, s34, s4
	s_cselect_b32 s45, s37, s31
	s_cselect_b32 s44, s36, s29
	s_add_i32 s74, 0, 0x14000
	v_add_u32_e32 v154, s69, v162
	v_add_u32_e32 v165, s74, v162
	ds_read_b128 v[132:135], v154
	ds_read_b128 v[136:139], v154 offset:1024
	ds_read_b128 v[140:143], v154 offset:2048
	ds_read_b128 v[154:157], v154 offset:3072
	ds_read_b128 v[158:161], v165
	ds_read_b128 v[166:169], v165 offset:1024
	ds_read_b128 v[170:173], v165 offset:2048
	ds_read_b128 v[174:177], v165 offset:3072
	v_lshl_add_u64 v[198:199], s[38:39], 0, v[152:153]
	s_add_i32 m0, s50, 0xc000
	ds_read_b128 v[178:181], v164
	ds_read_b128 v[182:185], v164 offset:1024
	ds_read_b128 v[186:189], v164 offset:2048
	ds_read_b128 v[190:193], v164 offset:3072
	ds_read_b128 v[194:197], v164 offset:4096
	ds_read_b128 v[224:227], v164 offset:5120
	ds_read_b128 v[228:231], v164 offset:6144
	ds_read_b128 v[238:241], v164 offset:7168
	global_load_lds_dwordx4 v[198:199], off
	v_lshl_add_u64 v[198:199], s[38:39], 0, v[150:151]
	s_add_i32 m0, s50, 0xe000
	s_nop 0
	global_load_lds_dwordx4 v[198:199], off
	s_waitcnt vmcnt(8)
	s_waitcnt lgkmcnt(0)
	s_barrier
	s_waitcnt lgkmcnt(0)
	v_mfma_f32_16x16x32_bf16 v[128:131], v[132:135], v[178:181], v[128:131]
	v_mfma_f32_16x16x32_bf16 v[124:127], v[140:143], v[178:181], v[124:127]
	v_mfma_f32_16x16x32_bf16 v[120:123], v[132:135], v[186:189], v[120:123]
	v_mfma_f32_16x16x32_bf16 v[108:111], v[140:143], v[186:189], v[108:111]
	v_mfma_f32_16x16x32_bf16 v[104:107], v[132:135], v[194:197], v[104:107]
	v_mfma_f32_16x16x32_bf16 v[92:95], v[140:143], v[194:197], v[92:95]
	v_mfma_f32_16x16x32_bf16 v[88:91], v[132:135], v[228:231], v[88:91]
	v_mfma_f32_16x16x32_bf16 v[76:79], v[140:143], v[228:231], v[76:79]
	v_mfma_f32_16x16x32_bf16 v[128:131], v[136:139], v[182:185], v[128:131]
	v_mfma_f32_16x16x32_bf16 v[124:127], v[154:157], v[182:185], v[124:127]
	v_mfma_f32_16x16x32_bf16 v[120:123], v[136:139], v[190:193], v[120:123]
	v_mfma_f32_16x16x32_bf16 v[108:111], v[154:157], v[190:193], v[108:111]
	v_mfma_f32_16x16x32_bf16 v[104:107], v[136:139], v[224:227], v[104:107]
	v_mfma_f32_16x16x32_bf16 v[92:95], v[154:157], v[224:227], v[92:95]
	v_mfma_f32_16x16x32_bf16 v[88:91], v[136:139], v[238:241], v[88:91]
	v_mfma_f32_16x16x32_bf16 v[76:79], v[154:157], v[238:241], v[76:79]
	v_mfma_f32_16x16x32_bf16 v[116:119], v[158:161], v[178:181], v[116:119]
	v_mfma_f32_16x16x32_bf16 v[112:115], v[170:173], v[178:181], v[112:115]
	v_mfma_f32_16x16x32_bf16 v[100:103], v[158:161], v[186:189], v[100:103]
	v_mfma_f32_16x16x32_bf16 v[96:99], v[170:173], v[186:189], v[96:99]
	v_mfma_f32_16x16x32_bf16 v[84:87], v[158:161], v[194:197], v[84:87]
	v_mfma_f32_16x16x32_bf16 v[80:83], v[170:173], v[194:197], v[80:83]
	v_mfma_f32_16x16x32_bf16 v[72:75], v[158:161], v[228:231], v[72:75]
	v_mfma_f32_16x16x32_bf16 v[68:71], v[170:173], v[228:231], v[68:71]
	v_mfma_f32_16x16x32_bf16 v[116:119], v[166:169], v[182:185], v[116:119]
	v_mfma_f32_16x16x32_bf16 v[112:115], v[174:177], v[182:185], v[112:115]
	v_mfma_f32_16x16x32_bf16 v[100:103], v[166:169], v[190:193], v[100:103]
	v_mfma_f32_16x16x32_bf16 v[96:99], v[174:177], v[190:193], v[96:99]
	v_mfma_f32_16x16x32_bf16 v[84:87], v[166:169], v[224:227], v[84:87]
	v_mfma_f32_16x16x32_bf16 v[80:83], v[174:177], v[224:227], v[80:83]
	v_mfma_f32_16x16x32_bf16 v[72:75], v[166:169], v[238:241], v[72:75]
	v_mfma_f32_16x16x32_bf16 v[68:71], v[174:177], v[238:241], v[68:71]
	s_barrier
	s_add_i32 s69, s69, s49
	v_lshl_add_u64 v[198:199], s[44:45], 0, v[34:35]
	s_mov_b32 m0, s69
	ds_read_b128 v[178:181], v164 offset:16384
	ds_read_b128 v[182:185], v164 offset:17408
	ds_read_b128 v[186:189], v164 offset:18432
	ds_read_b128 v[190:193], v164 offset:19456
	ds_read_b128 v[194:197], v164 offset:20480
	ds_read_b128 v[224:227], v164 offset:21504
	ds_read_b128 v[228:231], v164 offset:22528
	ds_read_b128 v[238:241], v164 offset:23552
	global_load_lds_dwordx4 v[198:199], off
	s_add_i32 m0, s69, 0x2000
	s_add_u32 s70, s44, 0x80000
	v_lshl_add_u64 v[212:213], s[44:45], 0, v[144:145]
	s_addc_u32 s71, s45, 0
	s_add_i32 s69, s74, s49
	global_load_lds_dwordx4 v[212:213], off
	v_lshl_add_u64 v[232:233], s[70:71], 0, v[34:35]
	s_mov_b32 m0, s69
	v_lshl_add_u64 v[242:243], s[4:5], 0, v[144:145]
	global_load_lds_dwordx4 v[232:233], off
	v_lshl_add_u64 v[232:233], s[70:71], 0, v[144:145]
	s_add_i32 m0, s69, 0x2000
	s_nop 0
	global_load_lds_dwordx4 v[232:233], off
	v_lshl_add_u64 v[232:233], s[4:5], 0, v[34:35]
	s_mov_b32 m0, s50
	s_nop 0
	global_load_lds_dwordx4 v[232:233], off
	s_mov_b32 m0, s51
	s_nop 0
	global_load_lds_dwordx4 v[242:243], off
	s_waitcnt vmcnt(8)
	s_waitcnt lgkmcnt(0)
	s_barrier
	s_waitcnt lgkmcnt(0)
	v_mfma_f32_16x16x32_bf16 v[64:67], v[132:135], v[178:181], v[64:67]
	v_mfma_f32_16x16x32_bf16 v[60:63], v[140:143], v[178:181], v[60:63]
	v_mfma_f32_16x16x32_bf16 v[56:59], v[132:135], v[186:189], v[56:59]
	v_mfma_f32_16x16x32_bf16 v[44:47], v[140:143], v[186:189], v[44:47]
	v_mfma_f32_16x16x32_bf16 v[40:43], v[132:135], v[194:197], v[40:43]
	v_mfma_f32_16x16x32_bf16 v[26:29], v[140:143], v[194:197], v[26:29]
	v_mfma_f32_16x16x32_bf16 v[22:25], v[132:135], v[228:231], v[22:25]
	v_mfma_f32_16x16x32_bf16 v[10:13], v[140:143], v[228:231], v[10:13]
	v_mfma_f32_16x16x32_bf16 v[64:67], v[136:139], v[182:185], v[64:67]
	v_mfma_f32_16x16x32_bf16 v[60:63], v[154:157], v[182:185], v[60:63]
	v_mfma_f32_16x16x32_bf16 v[56:59], v[136:139], v[190:193], v[56:59]
	v_mfma_f32_16x16x32_bf16 v[44:47], v[154:157], v[190:193], v[44:47]
	v_mfma_f32_16x16x32_bf16 v[40:43], v[136:139], v[224:227], v[40:43]
	v_mfma_f32_16x16x32_bf16 v[26:29], v[154:157], v[224:227], v[26:29]
	v_mfma_f32_16x16x32_bf16 v[22:25], v[136:139], v[238:241], v[22:25]
	v_mfma_f32_16x16x32_bf16 v[10:13], v[154:157], v[238:241], v[10:13]
	v_mfma_f32_16x16x32_bf16 v[52:55], v[158:161], v[178:181], v[52:55]
	v_mfma_f32_16x16x32_bf16 v[48:51], v[170:173], v[178:181], v[48:51]
	v_mfma_f32_16x16x32_bf16 v[36:39], v[158:161], v[186:189], v[36:39]
	v_mfma_f32_16x16x32_bf16 v[30:33], v[170:173], v[186:189], v[30:33]
	v_mfma_f32_16x16x32_bf16 v[18:21], v[158:161], v[194:197], v[18:21]
	v_mfma_f32_16x16x32_bf16 v[14:17], v[170:173], v[194:197], v[14:17]
	v_mfma_f32_16x16x32_bf16 v[6:9], v[158:161], v[228:231], v[6:9]
	v_mfma_f32_16x16x32_bf16 v[2:5], v[170:173], v[228:231], v[2:5]
	v_mfma_f32_16x16x32_bf16 v[52:55], v[166:169], v[182:185], v[52:55]
	v_mfma_f32_16x16x32_bf16 v[48:51], v[174:177], v[182:185], v[48:51]
	v_mfma_f32_16x16x32_bf16 v[36:39], v[166:169], v[190:193], v[36:39]
	v_mfma_f32_16x16x32_bf16 v[30:33], v[174:177], v[190:193], v[30:33]
	v_mfma_f32_16x16x32_bf16 v[18:21], v[166:169], v[224:227], v[18:21]
	v_mfma_f32_16x16x32_bf16 v[14:17], v[174:177], v[224:227], v[14:17]
	v_mfma_f32_16x16x32_bf16 v[6:9], v[166:169], v[238:241], v[6:9]
	v_mfma_f32_16x16x32_bf16 v[2:5], v[174:177], v[238:241], v[2:5]
	s_barrier
	s_add_i32 s69, 0, 0x18000
	s_add_i32 s70, 0, 0x1c000
	v_add_u32_e32 v154, s69, v162
	v_add_u32_e32 v165, s70, v162
	ds_read_b128 v[132:135], v154
	ds_read_b128 v[136:139], v154 offset:1024
	ds_read_b128 v[140:143], v154 offset:2048
	ds_read_b128 v[154:157], v154 offset:3072
	ds_read_b128 v[158:161], v165
	ds_read_b128 v[166:169], v165 offset:1024
	ds_read_b128 v[170:173], v165 offset:2048
	ds_read_b128 v[174:177], v165 offset:3072
	s_mov_b32 m0, s52
	v_lshl_add_u64 v[244:245], s[4:5], 0, v[148:149]
	ds_read_b128 v[178:181], v164 offset:32768
	ds_read_b128 v[182:185], v164 offset:33792
	ds_read_b128 v[186:189], v164 offset:34816
	ds_read_b128 v[190:193], v164 offset:35840
	ds_read_b128 v[194:197], v164 offset:36864
	ds_read_b128 v[224:227], v164 offset:37888
	ds_read_b128 v[228:231], v164 offset:38912
	ds_read_b128 v[238:241], v164 offset:39936
	global_load_lds_dwordx4 v[244:245], off
	v_lshl_add_u64 v[244:245], s[4:5], 0, v[146:147]
	s_mov_b32 m0, s53
	s_nop 0
	global_load_lds_dwordx4 v[244:245], off
	s_waitcnt vmcnt(8)
	s_waitcnt lgkmcnt(0)
	s_barrier
	s_waitcnt lgkmcnt(0)
	v_mfma_f32_16x16x32_bf16 v[128:131], v[132:135], v[178:181], v[128:131]
	v_mfma_f32_16x16x32_bf16 v[124:127], v[140:143], v[178:181], v[124:127]
	v_mfma_f32_16x16x32_bf16 v[120:123], v[132:135], v[186:189], v[120:123]
	v_mfma_f32_16x16x32_bf16 v[108:111], v[140:143], v[186:189], v[108:111]
	v_mfma_f32_16x16x32_bf16 v[104:107], v[132:135], v[194:197], v[104:107]
	v_mfma_f32_16x16x32_bf16 v[92:95], v[140:143], v[194:197], v[92:95]
	v_mfma_f32_16x16x32_bf16 v[88:91], v[132:135], v[228:231], v[88:91]
	v_mfma_f32_16x16x32_bf16 v[76:79], v[140:143], v[228:231], v[76:79]
	v_mfma_f32_16x16x32_bf16 v[128:131], v[136:139], v[182:185], v[128:131]
	v_mfma_f32_16x16x32_bf16 v[124:127], v[154:157], v[182:185], v[124:127]
	v_mfma_f32_16x16x32_bf16 v[120:123], v[136:139], v[190:193], v[120:123]
	v_mfma_f32_16x16x32_bf16 v[108:111], v[154:157], v[190:193], v[108:111]
	v_mfma_f32_16x16x32_bf16 v[104:107], v[136:139], v[224:227], v[104:107]
	v_mfma_f32_16x16x32_bf16 v[92:95], v[154:157], v[224:227], v[92:95]
	v_mfma_f32_16x16x32_bf16 v[88:91], v[136:139], v[238:241], v[88:91]
	v_mfma_f32_16x16x32_bf16 v[76:79], v[154:157], v[238:241], v[76:79]
	v_mfma_f32_16x16x32_bf16 v[116:119], v[158:161], v[178:181], v[116:119]
	v_mfma_f32_16x16x32_bf16 v[112:115], v[170:173], v[178:181], v[112:115]
	v_mfma_f32_16x16x32_bf16 v[100:103], v[158:161], v[186:189], v[100:103]
	v_mfma_f32_16x16x32_bf16 v[96:99], v[170:173], v[186:189], v[96:99]
	v_mfma_f32_16x16x32_bf16 v[84:87], v[158:161], v[194:197], v[84:87]
	v_mfma_f32_16x16x32_bf16 v[80:83], v[170:173], v[194:197], v[80:83]
	v_mfma_f32_16x16x32_bf16 v[72:75], v[158:161], v[228:231], v[72:75]
	v_mfma_f32_16x16x32_bf16 v[68:71], v[170:173], v[228:231], v[68:71]
	v_mfma_f32_16x16x32_bf16 v[116:119], v[166:169], v[182:185], v[116:119]
	v_mfma_f32_16x16x32_bf16 v[112:115], v[174:177], v[182:185], v[112:115]
	v_mfma_f32_16x16x32_bf16 v[100:103], v[166:169], v[190:193], v[100:103]
	v_mfma_f32_16x16x32_bf16 v[96:99], v[174:177], v[190:193], v[96:99]
	v_mfma_f32_16x16x32_bf16 v[84:87], v[166:169], v[224:227], v[84:87]
	v_mfma_f32_16x16x32_bf16 v[80:83], v[174:177], v[224:227], v[80:83]
	v_mfma_f32_16x16x32_bf16 v[72:75], v[166:169], v[238:241], v[72:75]
	v_mfma_f32_16x16x32_bf16 v[68:71], v[174:177], v[238:241], v[68:71]
	s_barrier
	s_add_i32 s4, s69, s49
	v_lshl_add_u64 v[198:199], v[198:199], 0, s[78:79]
	s_mov_b32 m0, s4
	ds_read_b128 v[178:181], v164 offset:49152
	ds_read_b128 v[182:185], v164 offset:50176
	ds_read_b128 v[186:189], v164 offset:51200
	ds_read_b128 v[190:193], v164 offset:52224
	ds_read_b128 v[194:197], v164 offset:53248
	ds_read_b128 v[224:227], v164 offset:54272
	ds_read_b128 v[228:231], v164 offset:55296
	ds_read_b128 v[238:241], v164 offset:56320
	global_load_lds_dwordx4 v[198:199], off
	s_add_i32 m0, s4, 0x2000
	s_add_u32 s4, s44, 0x80080
	v_lshl_add_u64 v[198:199], v[212:213], 0, s[78:79]
	s_addc_u32 s5, s45, 0
	s_add_i32 s44, s70, s49
	global_load_lds_dwordx4 v[198:199], off
	v_lshl_add_u64 v[198:199], s[4:5], 0, v[34:35]
	s_mov_b32 m0, s44
	s_nop 0
	global_load_lds_dwordx4 v[198:199], off
	v_lshl_add_u64 v[198:199], s[4:5], 0, v[144:145]
	s_add_i32 m0, s44, 0x2000
	s_nop 0
	global_load_lds_dwordx4 v[198:199], off
	v_lshl_add_u64 v[198:199], v[232:233], 0, s[78:79]
	s_mov_b32 m0, s54
	s_nop 0
	global_load_lds_dwordx4 v[198:199], off
	v_lshl_add_u64 v[198:199], v[242:243], 0, s[78:79]
	s_mov_b32 m0, s55
	s_nop 0
	global_load_lds_dwordx4 v[198:199], off
	s_waitcnt vmcnt(8)
	s_waitcnt lgkmcnt(0)
	s_barrier
	s_waitcnt lgkmcnt(0)
	v_mfma_f32_16x16x32_bf16 v[64:67], v[132:135], v[178:181], v[64:67]
	v_mfma_f32_16x16x32_bf16 v[60:63], v[140:143], v[178:181], v[60:63]
	v_mfma_f32_16x16x32_bf16 v[56:59], v[132:135], v[186:189], v[56:59]
	v_mfma_f32_16x16x32_bf16 v[44:47], v[140:143], v[186:189], v[44:47]
	v_mfma_f32_16x16x32_bf16 v[40:43], v[132:135], v[194:197], v[40:43]
	v_mfma_f32_16x16x32_bf16 v[26:29], v[140:143], v[194:197], v[26:29]
	v_mfma_f32_16x16x32_bf16 v[22:25], v[132:135], v[228:231], v[22:25]
	v_mfma_f32_16x16x32_bf16 v[10:13], v[140:143], v[228:231], v[10:13]
	v_mfma_f32_16x16x32_bf16 v[64:67], v[136:139], v[182:185], v[64:67]
	v_mfma_f32_16x16x32_bf16 v[60:63], v[154:157], v[182:185], v[60:63]
	v_mfma_f32_16x16x32_bf16 v[56:59], v[136:139], v[190:193], v[56:59]
	v_mfma_f32_16x16x32_bf16 v[44:47], v[154:157], v[190:193], v[44:47]
	v_mfma_f32_16x16x32_bf16 v[40:43], v[136:139], v[224:227], v[40:43]
	v_mfma_f32_16x16x32_bf16 v[26:29], v[154:157], v[224:227], v[26:29]
	v_mfma_f32_16x16x32_bf16 v[22:25], v[136:139], v[238:241], v[22:25]
	v_mfma_f32_16x16x32_bf16 v[10:13], v[154:157], v[238:241], v[10:13]
	v_mfma_f32_16x16x32_bf16 v[52:55], v[158:161], v[178:181], v[52:55]
	v_mfma_f32_16x16x32_bf16 v[48:51], v[170:173], v[178:181], v[48:51]
	v_mfma_f32_16x16x32_bf16 v[36:39], v[158:161], v[186:189], v[36:39]
	v_mfma_f32_16x16x32_bf16 v[30:33], v[170:173], v[186:189], v[30:33]
	v_mfma_f32_16x16x32_bf16 v[18:21], v[158:161], v[194:197], v[18:21]
	v_mfma_f32_16x16x32_bf16 v[14:17], v[170:173], v[194:197], v[14:17]
	v_mfma_f32_16x16x32_bf16 v[6:9], v[158:161], v[228:231], v[6:9]
	v_mfma_f32_16x16x32_bf16 v[2:5], v[170:173], v[228:231], v[2:5]
	v_mfma_f32_16x16x32_bf16 v[52:55], v[166:169], v[182:185], v[52:55]
	v_mfma_f32_16x16x32_bf16 v[48:51], v[174:177], v[182:185], v[48:51]
	v_mfma_f32_16x16x32_bf16 v[36:39], v[166:169], v[190:193], v[36:39]
	v_mfma_f32_16x16x32_bf16 v[30:33], v[174:177], v[190:193], v[30:33]
	v_mfma_f32_16x16x32_bf16 v[18:21], v[166:169], v[224:227], v[18:21]
	v_mfma_f32_16x16x32_bf16 v[14:17], v[174:177], v[224:227], v[14:17]
	v_mfma_f32_16x16x32_bf16 v[6:9], v[166:169], v[238:241], v[6:9]
	v_mfma_f32_16x16x32_bf16 v[2:5], v[174:177], v[238:241], v[2:5]
	s_barrier
	s_add_i32 s68, s68, 2
	s_add_u32 s29, s29, 0x100
	s_addc_u32 s31, s31, 0
	s_add_u32 s38, s38, 0x100
	s_addc_u32 s39, s39, 0
	s_cmp_gt_u32 s68, 29
	s_cbranch_scc0 .LBB0_787
	s_setprio 0
	s_and_b64 vcc, exec, s[26:27]
	s_cbranch_vccz .LBB0_790
	s_barrier

.LBB0_1198:
	s_add_u32 s50, s36, 0x100
	s_addc_u32 s51, s37, 0
	s_add_u32 s34, s34, 0x80
	v_mov_b32_e32 v2, 0
	s_addc_u32 s35, s35, 0
	s_mov_b32 s52, -2
	v_mov_b32_e32 v3, v2
	v_mov_b32_e32 v4, v2
	v_mov_b32_e32 v5, v2
	v_mov_b32_e32 v6, v2
	v_mov_b32_e32 v7, v2
	v_mov_b32_e32 v8, v2
	v_mov_b32_e32 v9, v2
	v_mov_b32_e32 v14, v2
	v_mov_b32_e32 v15, v2
	v_mov_b32_e32 v16, v2
	v_mov_b32_e32 v17, v2
	v_mov_b32_e32 v22, v2
	v_mov_b32_e32 v23, v2
	v_mov_b32_e32 v24, v2
	v_mov_b32_e32 v25, v2
	v_mov_b32_e32 v30, v2
	v_mov_b32_e32 v31, v2
	v_mov_b32_e32 v32, v2
	v_mov_b32_e32 v33, v2
	v_mov_b32_e32 v40, v2
	v_mov_b32_e32 v41, v2
	v_mov_b32_e32 v42, v2
	v_mov_b32_e32 v43, v2
	v_mov_b32_e32 v48, v2
	v_mov_b32_e32 v49, v2
	v_mov_b32_e32 v50, v2
	v_mov_b32_e32 v51, v2
	v_mov_b32_e32 v56, v2
	v_mov_b32_e32 v57, v2
	v_mov_b32_e32 v58, v2
	v_mov_b32_e32 v59, v2
	v_mov_b32_e32 v10, v2
	v_mov_b32_e32 v11, v2
	v_mov_b32_e32 v12, v2
	v_mov_b32_e32 v13, v2
	v_mov_b32_e32 v18, v2
	v_mov_b32_e32 v19, v2
	v_mov_b32_e32 v20, v2
	v_mov_b32_e32 v21, v2
	v_mov_b32_e32 v26, v2
	v_mov_b32_e32 v27, v2
	v_mov_b32_e32 v28, v2
	v_mov_b32_e32 v29, v2
	v_mov_b32_e32 v36, v2
	v_mov_b32_e32 v37, v2
	v_mov_b32_e32 v38, v2
	v_mov_b32_e32 v39, v2
	v_mov_b32_e32 v44, v2
	v_mov_b32_e32 v45, v2
	v_mov_b32_e32 v46, v2
	v_mov_b32_e32 v47, v2
	v_mov_b32_e32 v52, v2
	v_mov_b32_e32 v53, v2
	v_mov_b32_e32 v54, v2
	v_mov_b32_e32 v55, v2
	v_mov_b32_e32 v60, v2
	v_mov_b32_e32 v61, v2
	v_mov_b32_e32 v62, v2
	v_mov_b32_e32 v63, v2
	v_mov_b32_e32 v64, v2
	v_mov_b32_e32 v65, v2
	v_mov_b32_e32 v66, v2
	v_mov_b32_e32 v67, v2
	v_mov_b32_e32 v68, v2
	v_mov_b32_e32 v69, v2
	v_mov_b32_e32 v70, v2
	v_mov_b32_e32 v71, v2
	v_mov_b32_e32 v72, v2
	v_mov_b32_e32 v73, v2
	v_mov_b32_e32 v74, v2
	v_mov_b32_e32 v75, v2
	v_mov_b32_e32 v80, v2
	v_mov_b32_e32 v81, v2
	v_mov_b32_e32 v82, v2
	v_mov_b32_e32 v83, v2
	v_mov_b32_e32 v88, v2
	v_mov_b32_e32 v89, v2
	v_mov_b32_e32 v90, v2
	v_mov_b32_e32 v91, v2
	v_mov_b32_e32 v96, v2
	v_mov_b32_e32 v97, v2
	v_mov_b32_e32 v98, v2
	v_mov_b32_e32 v99, v2
	v_mov_b32_e32 v104, v2
	v_mov_b32_e32 v105, v2
	v_mov_b32_e32 v106, v2
	v_mov_b32_e32 v107, v2
	v_mov_b32_e32 v112, v2
	v_mov_b32_e32 v113, v2
	v_mov_b32_e32 v114, v2
	v_mov_b32_e32 v115, v2
	v_mov_b32_e32 v120, v2
	v_mov_b32_e32 v121, v2
	v_mov_b32_e32 v122, v2
	v_mov_b32_e32 v123, v2
	v_mov_b32_e32 v76, v2
	v_mov_b32_e32 v77, v2
	v_mov_b32_e32 v78, v2
	v_mov_b32_e32 v79, v2
	v_mov_b32_e32 v84, v2
	v_mov_b32_e32 v85, v2
	v_mov_b32_e32 v86, v2
	v_mov_b32_e32 v87, v2
	v_mov_b32_e32 v92, v2
	v_mov_b32_e32 v93, v2
	v_mov_b32_e32 v94, v2
	v_mov_b32_e32 v95, v2
	v_mov_b32_e32 v100, v2
	v_mov_b32_e32 v101, v2
	v_mov_b32_e32 v102, v2
	v_mov_b32_e32 v103, v2
	v_mov_b32_e32 v108, v2
	v_mov_b32_e32 v109, v2
	v_mov_b32_e32 v110, v2
	v_mov_b32_e32 v111, v2
	v_mov_b32_e32 v116, v2
	v_mov_b32_e32 v117, v2
	v_mov_b32_e32 v118, v2
	v_mov_b32_e32 v119, v2
	v_mov_b32_e32 v124, v2
	v_mov_b32_e32 v125, v2
	v_mov_b32_e32 v126, v2
	v_mov_b32_e32 v127, v2
	v_mov_b32_e32 v128, v2
	v_mov_b32_e32 v129, v2
	v_mov_b32_e32 v130, v2
	v_mov_b32_e32 v131, v2
	v_readfirstlane_b32 s96, v0
	s_nop 3
	s_bitcmp1_b32 s96, 8
	s_cbranch_scc0 .Lsp1199
	s_setprio 1
.Lsp1199:
.LBB0_1199:
	s_add_u32 s4, s34, 0x80
	s_addc_u32 s5, s35, 0
	s_add_i32 s53, 0, 0x10000
	s_cmp_eq_u32 s52, 4
	s_cselect_b32 s5, s27, s5
	s_cselect_b32 s4, s26, s4
	v_add_u32_e32 v34, s53, v1
	s_cselect_b32 s37, s29, s51
	s_cselect_b32 s36, s28, s50
	s_add_i32 s56, 0, 0x14000
	ds_read_b128 v[154:157], v34
	ds_read_b128 v[158:161], v34 offset:1024
	ds_read_b128 v[162:165], v34 offset:2048
	ds_read_b128 v[166:169], v34 offset:3072
	v_add_u32_e32 v34, s56, v1
	ds_read_b128 v[170:173], v34
	ds_read_b128 v[174:177], v34 offset:1024
	ds_read_b128 v[178:181], v34 offset:2048
	ds_read_b128 v[182:185], v34 offset:3072
	v_lshl_add_u64 v[148:149], s[34:35], 0, v[146:147]
	s_add_i32 m0, s41, 0xc000
	ds_read_b128 v[186:189], v152
	ds_read_b128 v[190:193], v152 offset:1024
	ds_read_b128 v[194:197], v152 offset:2048
	ds_read_b128 v[224:227], v152 offset:3072
	ds_read_b128 v[228:231], v152 offset:4096
	ds_read_b128 v[238:241], v152 offset:5120
	ds_read_b128 v[242:245], v152 offset:6144
	ds_read_b128 v[246:249], v152 offset:7168
	global_load_lds_dwordx4 v[148:149], off
	v_lshl_add_u64 v[148:149], s[34:35], 0, v[144:145]
	s_add_i32 m0, s41, 0xe000
	s_nop 0
	global_load_lds_dwordx4 v[148:149], off
	s_waitcnt vmcnt(8)
	s_waitcnt lgkmcnt(0)
	s_barrier
	s_waitcnt lgkmcnt(0)
	v_mfma_f32_16x16x32_bf16 v[128:131], v[154:157], v[186:189], v[128:131]
	v_mfma_f32_16x16x32_bf16 v[124:127], v[162:165], v[186:189], v[124:127]
	v_mfma_f32_16x16x32_bf16 v[116:119], v[154:157], v[194:197], v[116:119]
	v_mfma_f32_16x16x32_bf16 v[108:111], v[162:165], v[194:197], v[108:111]
	v_mfma_f32_16x16x32_bf16 v[100:103], v[154:157], v[228:231], v[100:103]
	v_mfma_f32_16x16x32_bf16 v[92:95], v[162:165], v[228:231], v[92:95]
	v_mfma_f32_16x16x32_bf16 v[84:87], v[154:157], v[242:245], v[84:87]
	v_mfma_f32_16x16x32_bf16 v[76:79], v[162:165], v[242:245], v[76:79]
	v_mfma_f32_16x16x32_bf16 v[128:131], v[158:161], v[190:193], v[128:131]
	v_mfma_f32_16x16x32_bf16 v[124:127], v[166:169], v[190:193], v[124:127]
	v_mfma_f32_16x16x32_bf16 v[116:119], v[158:161], v[224:227], v[116:119]
	v_mfma_f32_16x16x32_bf16 v[108:111], v[166:169], v[224:227], v[108:111]
	v_mfma_f32_16x16x32_bf16 v[100:103], v[158:161], v[238:241], v[100:103]
	v_mfma_f32_16x16x32_bf16 v[92:95], v[166:169], v[238:241], v[92:95]
	v_mfma_f32_16x16x32_bf16 v[84:87], v[158:161], v[246:249], v[84:87]
	v_mfma_f32_16x16x32_bf16 v[76:79], v[166:169], v[246:249], v[76:79]
	v_mfma_f32_16x16x32_bf16 v[120:123], v[170:173], v[186:189], v[120:123]
	v_mfma_f32_16x16x32_bf16 v[112:115], v[178:181], v[186:189], v[112:115]
	v_mfma_f32_16x16x32_bf16 v[104:107], v[170:173], v[194:197], v[104:107]
	v_mfma_f32_16x16x32_bf16 v[96:99], v[178:181], v[194:197], v[96:99]
	v_mfma_f32_16x16x32_bf16 v[88:91], v[170:173], v[228:231], v[88:91]
	v_mfma_f32_16x16x32_bf16 v[80:83], v[178:181], v[228:231], v[80:83]
	v_mfma_f32_16x16x32_bf16 v[72:75], v[170:173], v[242:245], v[72:75]
	v_mfma_f32_16x16x32_bf16 v[68:71], v[178:181], v[242:245], v[68:71]
	v_mfma_f32_16x16x32_bf16 v[120:123], v[174:177], v[190:193], v[120:123]
	v_mfma_f32_16x16x32_bf16 v[112:115], v[182:185], v[190:193], v[112:115]
	v_mfma_f32_16x16x32_bf16 v[104:107], v[174:177], v[224:227], v[104:107]
	v_mfma_f32_16x16x32_bf16 v[96:99], v[182:185], v[224:227], v[96:99]
	v_mfma_f32_16x16x32_bf16 v[88:91], v[174:177], v[238:241], v[88:91]
	v_mfma_f32_16x16x32_bf16 v[80:83], v[182:185], v[238:241], v[80:83]
	v_mfma_f32_16x16x32_bf16 v[72:75], v[174:177], v[246:249], v[72:75]
	v_mfma_f32_16x16x32_bf16 v[68:71], v[182:185], v[246:249], v[68:71]
	s_barrier
	s_add_i32 s53, s53, s14
	v_lshl_add_u64 v[148:149], s[36:37], 0, v[138:139]
	s_mov_b32 m0, s53
	ds_read_b128 v[186:189], v152 offset:16384
	ds_read_b128 v[190:193], v152 offset:17408
	ds_read_b128 v[194:197], v152 offset:18432
	ds_read_b128 v[224:227], v152 offset:19456
	ds_read_b128 v[228:231], v152 offset:20480
	ds_read_b128 v[238:241], v152 offset:21504
	ds_read_b128 v[242:245], v152 offset:22528
	ds_read_b128 v[246:249], v152 offset:23552
	global_load_lds_dwordx4 v[148:149], off
	s_add_i32 m0, s53, 0x2000
	s_add_u32 s54, s36, 0x20000
	v_lshl_add_u64 v[198:199], s[36:37], 0, v[132:133]
	s_addc_u32 s55, s37, 0
	s_add_i32 s53, s56, s14
	global_load_lds_dwordx4 v[198:199], off
	v_lshl_add_u64 v[208:209], s[54:55], 0, v[138:139]
	s_mov_b32 m0, s53
	v_lshl_add_u64 v[212:213], s[4:5], 0, v[134:135]
	global_load_lds_dwordx4 v[208:209], off
	v_lshl_add_u64 v[208:209], s[54:55], 0, v[132:133]
	s_add_i32 m0, s53, 0x2000
	s_nop 0
	global_load_lds_dwordx4 v[208:209], off
	v_lshl_add_u64 v[208:209], s[4:5], 0, v[140:141]
	s_mov_b32 m0, s41
	s_nop 0
	global_load_lds_dwordx4 v[208:209], off
	s_mov_b32 m0, s42
	s_nop 0
	global_load_lds_dwordx4 v[212:213], off
	s_waitcnt vmcnt(8)
	s_waitcnt lgkmcnt(0)
	s_barrier
	s_waitcnt lgkmcnt(0)
	v_mfma_f32_16x16x32_bf16 v[64:67], v[154:157], v[186:189], v[64:67]
	v_mfma_f32_16x16x32_bf16 v[60:63], v[162:165], v[186:189], v[60:63]
	v_mfma_f32_16x16x32_bf16 v[52:55], v[154:157], v[194:197], v[52:55]
	v_mfma_f32_16x16x32_bf16 v[44:47], v[162:165], v[194:197], v[44:47]
	v_mfma_f32_16x16x32_bf16 v[36:39], v[154:157], v[228:231], v[36:39]
	v_mfma_f32_16x16x32_bf16 v[26:29], v[162:165], v[228:231], v[26:29]
	v_mfma_f32_16x16x32_bf16 v[18:21], v[154:157], v[242:245], v[18:21]
	v_mfma_f32_16x16x32_bf16 v[10:13], v[162:165], v[242:245], v[10:13]
	v_mfma_f32_16x16x32_bf16 v[64:67], v[158:161], v[190:193], v[64:67]
	v_mfma_f32_16x16x32_bf16 v[60:63], v[166:169], v[190:193], v[60:63]
	v_mfma_f32_16x16x32_bf16 v[52:55], v[158:161], v[224:227], v[52:55]
	v_mfma_f32_16x16x32_bf16 v[44:47], v[166:169], v[224:227], v[44:47]
	v_mfma_f32_16x16x32_bf16 v[36:39], v[158:161], v[238:241], v[36:39]
	v_mfma_f32_16x16x32_bf16 v[26:29], v[166:169], v[238:241], v[26:29]
	v_mfma_f32_16x16x32_bf16 v[18:21], v[158:161], v[246:249], v[18:21]
	v_mfma_f32_16x16x32_bf16 v[10:13], v[166:169], v[246:249], v[10:13]
	v_mfma_f32_16x16x32_bf16 v[56:59], v[170:173], v[186:189], v[56:59]
	v_mfma_f32_16x16x32_bf16 v[48:51], v[178:181], v[186:189], v[48:51]
	v_mfma_f32_16x16x32_bf16 v[40:43], v[170:173], v[194:197], v[40:43]
	v_mfma_f32_16x16x32_bf16 v[30:33], v[178:181], v[194:197], v[30:33]
	v_mfma_f32_16x16x32_bf16 v[22:25], v[170:173], v[228:231], v[22:25]
	v_mfma_f32_16x16x32_bf16 v[14:17], v[178:181], v[228:231], v[14:17]
	v_mfma_f32_16x16x32_bf16 v[6:9], v[170:173], v[242:245], v[6:9]
	v_mfma_f32_16x16x32_bf16 v[2:5], v[178:181], v[242:245], v[2:5]
	v_mfma_f32_16x16x32_bf16 v[56:59], v[174:177], v[190:193], v[56:59]
	v_mfma_f32_16x16x32_bf16 v[48:51], v[182:185], v[190:193], v[48:51]
	v_mfma_f32_16x16x32_bf16 v[40:43], v[174:177], v[224:227], v[40:43]
	v_mfma_f32_16x16x32_bf16 v[30:33], v[182:185], v[224:227], v[30:33]
	v_mfma_f32_16x16x32_bf16 v[22:25], v[174:177], v[238:241], v[22:25]
	v_mfma_f32_16x16x32_bf16 v[14:17], v[182:185], v[238:241], v[14:17]
	v_mfma_f32_16x16x32_bf16 v[6:9], v[174:177], v[246:249], v[6:9]
	v_mfma_f32_16x16x32_bf16 v[2:5], v[182:185], v[246:249], v[2:5]
	s_barrier
	s_add_i32 s53, 0, 0x18000
	v_add_u32_e32 v34, s53, v1
	s_add_i32 s54, 0, 0x1c000
	ds_read_b128 v[154:157], v34
	ds_read_b128 v[158:161], v34 offset:1024
	ds_read_b128 v[162:165], v34 offset:2048
	ds_read_b128 v[166:169], v34 offset:3072
	v_add_u32_e32 v34, s54, v1
	ds_read_b128 v[170:173], v34
	ds_read_b128 v[174:177], v34 offset:1024
	ds_read_b128 v[178:181], v34 offset:2048
	ds_read_b128 v[182:185], v34 offset:3072
	s_mov_b32 m0, s43
	v_lshl_add_u64 v[232:233], s[4:5], 0, v[142:143]
	ds_read_b128 v[186:189], v152 offset:32768
	ds_read_b128 v[190:193], v152 offset:33792
	ds_read_b128 v[194:197], v152 offset:34816
	ds_read_b128 v[224:227], v152 offset:35840
	ds_read_b128 v[228:231], v152 offset:36864
	ds_read_b128 v[238:241], v152 offset:37888
	ds_read_b128 v[242:245], v152 offset:38912
	ds_read_b128 v[246:249], v152 offset:39936
	global_load_lds_dwordx4 v[232:233], off
	v_lshl_add_u64 v[232:233], s[4:5], 0, v[136:137]
	s_mov_b32 m0, s44
	s_nop 0
	global_load_lds_dwordx4 v[232:233], off
	s_waitcnt vmcnt(8)
	s_waitcnt lgkmcnt(0)
	s_barrier
	s_waitcnt lgkmcnt(0)
	v_mfma_f32_16x16x32_bf16 v[128:131], v[154:157], v[186:189], v[128:131]
	v_mfma_f32_16x16x32_bf16 v[124:127], v[162:165], v[186:189], v[124:127]
	v_mfma_f32_16x16x32_bf16 v[116:119], v[154:157], v[194:197], v[116:119]
	v_mfma_f32_16x16x32_bf16 v[108:111], v[162:165], v[194:197], v[108:111]
	v_mfma_f32_16x16x32_bf16 v[100:103], v[154:157], v[228:231], v[100:103]
	v_mfma_f32_16x16x32_bf16 v[92:95], v[162:165], v[228:231], v[92:95]
	v_mfma_f32_16x16x32_bf16 v[84:87], v[154:157], v[242:245], v[84:87]
	v_mfma_f32_16x16x32_bf16 v[76:79], v[162:165], v[242:245], v[76:79]
	v_mfma_f32_16x16x32_bf16 v[128:131], v[158:161], v[190:193], v[128:131]
	v_mfma_f32_16x16x32_bf16 v[124:127], v[166:169], v[190:193], v[124:127]
	v_mfma_f32_16x16x32_bf16 v[116:119], v[158:161], v[224:227], v[116:119]
	v_mfma_f32_16x16x32_bf16 v[108:111], v[166:169], v[224:227], v[108:111]
	v_mfma_f32_16x16x32_bf16 v[100:103], v[158:161], v[238:241], v[100:103]
	v_mfma_f32_16x16x32_bf16 v[92:95], v[166:169], v[238:241], v[92:95]
	v_mfma_f32_16x16x32_bf16 v[84:87], v[158:161], v[246:249], v[84:87]
	v_mfma_f32_16x16x32_bf16 v[76:79], v[166:169], v[246:249], v[76:79]
	v_mfma_f32_16x16x32_bf16 v[120:123], v[170:173], v[186:189], v[120:123]
	v_mfma_f32_16x16x32_bf16 v[112:115], v[178:181], v[186:189], v[112:115]
	v_mfma_f32_16x16x32_bf16 v[104:107], v[170:173], v[194:197], v[104:107]
	v_mfma_f32_16x16x32_bf16 v[96:99], v[178:181], v[194:197], v[96:99]
	v_mfma_f32_16x16x32_bf16 v[88:91], v[170:173], v[228:231], v[88:91]
	v_mfma_f32_16x16x32_bf16 v[80:83], v[178:181], v[228:231], v[80:83]
	v_mfma_f32_16x16x32_bf16 v[72:75], v[170:173], v[242:245], v[72:75]
	v_mfma_f32_16x16x32_bf16 v[68:71], v[178:181], v[242:245], v[68:71]
	v_mfma_f32_16x16x32_bf16 v[120:123], v[174:177], v[190:193], v[120:123]
	v_mfma_f32_16x16x32_bf16 v[112:115], v[182:185], v[190:193], v[112:115]
	v_mfma_f32_16x16x32_bf16 v[104:107], v[174:177], v[224:227], v[104:107]
	v_mfma_f32_16x16x32_bf16 v[96:99], v[182:185], v[224:227], v[96:99]
	v_mfma_f32_16x16x32_bf16 v[88:91], v[174:177], v[238:241], v[88:91]
	v_mfma_f32_16x16x32_bf16 v[80:83], v[182:185], v[238:241], v[80:83]
	v_mfma_f32_16x16x32_bf16 v[72:75], v[174:177], v[246:249], v[72:75]
	v_mfma_f32_16x16x32_bf16 v[68:71], v[182:185], v[246:249], v[68:71]
	s_barrier
	s_add_i32 s4, s53, s14
	v_lshl_add_u64 v[148:149], v[148:149], 0, s[78:79]
	s_mov_b32 m0, s4
	ds_read_b128 v[186:189], v152 offset:49152
	ds_read_b128 v[190:193], v152 offset:50176
	ds_read_b128 v[194:197], v152 offset:51200
	ds_read_b128 v[224:227], v152 offset:52224
	ds_read_b128 v[228:231], v152 offset:53248
	ds_read_b128 v[238:241], v152 offset:54272
	ds_read_b128 v[242:245], v152 offset:55296
	ds_read_b128 v[246:249], v152 offset:56320
	global_load_lds_dwordx4 v[148:149], off
	s_add_i32 m0, s4, 0x2000
	s_add_u32 s4, s36, 0x20080
	v_lshl_add_u64 v[148:149], v[198:199], 0, s[78:79]
	s_addc_u32 s5, s37, 0
	s_add_i32 s36, s54, s14
	global_load_lds_dwordx4 v[148:149], off
	v_lshl_add_u64 v[148:149], s[4:5], 0, v[138:139]
	s_mov_b32 m0, s36
	s_nop 0
	global_load_lds_dwordx4 v[148:149], off
	v_lshl_add_u64 v[148:149], s[4:5], 0, v[132:133]
	s_add_i32 m0, s36, 0x2000
	s_nop 0
	global_load_lds_dwordx4 v[148:149], off
	v_lshl_add_u64 v[148:149], v[208:209], 0, s[78:79]
	s_mov_b32 m0, s45
	s_nop 0
	global_load_lds_dwordx4 v[148:149], off
	v_lshl_add_u64 v[148:149], v[212:213], 0, s[78:79]
	s_mov_b32 m0, s46
	s_nop 0
	global_load_lds_dwordx4 v[148:149], off
	s_waitcnt vmcnt(8)
	s_waitcnt lgkmcnt(0)
	s_barrier
	s_waitcnt lgkmcnt(0)
	v_mfma_f32_16x16x32_bf16 v[64:67], v[154:157], v[186:189], v[64:67]
	v_mfma_f32_16x16x32_bf16 v[60:63], v[162:165], v[186:189], v[60:63]
	v_mfma_f32_16x16x32_bf16 v[52:55], v[154:157], v[194:197], v[52:55]
	v_mfma_f32_16x16x32_bf16 v[44:47], v[162:165], v[194:197], v[44:47]
	v_mfma_f32_16x16x32_bf16 v[36:39], v[154:157], v[228:231], v[36:39]
	v_mfma_f32_16x16x32_bf16 v[26:29], v[162:165], v[228:231], v[26:29]
	v_mfma_f32_16x16x32_bf16 v[18:21], v[154:157], v[242:245], v[18:21]
	v_mfma_f32_16x16x32_bf16 v[10:13], v[162:165], v[242:245], v[10:13]
	v_mfma_f32_16x16x32_bf16 v[64:67], v[158:161], v[190:193], v[64:67]
	v_mfma_f32_16x16x32_bf16 v[60:63], v[166:169], v[190:193], v[60:63]
	v_mfma_f32_16x16x32_bf16 v[52:55], v[158:161], v[224:227], v[52:55]
	v_mfma_f32_16x16x32_bf16 v[44:47], v[166:169], v[224:227], v[44:47]
	v_mfma_f32_16x16x32_bf16 v[36:39], v[158:161], v[238:241], v[36:39]
	v_mfma_f32_16x16x32_bf16 v[26:29], v[166:169], v[238:241], v[26:29]
	v_mfma_f32_16x16x32_bf16 v[18:21], v[158:161], v[246:249], v[18:21]
	v_mfma_f32_16x16x32_bf16 v[10:13], v[166:169], v[246:249], v[10:13]
	v_mfma_f32_16x16x32_bf16 v[56:59], v[170:173], v[186:189], v[56:59]
	v_mfma_f32_16x16x32_bf16 v[48:51], v[178:181], v[186:189], v[48:51]
	v_mfma_f32_16x16x32_bf16 v[40:43], v[170:173], v[194:197], v[40:43]
	v_mfma_f32_16x16x32_bf16 v[30:33], v[178:181], v[194:197], v[30:33]
	v_mfma_f32_16x16x32_bf16 v[22:25], v[170:173], v[228:231], v[22:25]
	v_mfma_f32_16x16x32_bf16 v[14:17], v[178:181], v[228:231], v[14:17]
	v_mfma_f32_16x16x32_bf16 v[6:9], v[170:173], v[242:245], v[6:9]
	v_mfma_f32_16x16x32_bf16 v[2:5], v[178:181], v[242:245], v[2:5]
	v_mfma_f32_16x16x32_bf16 v[56:59], v[174:177], v[190:193], v[56:59]
	v_mfma_f32_16x16x32_bf16 v[48:51], v[182:185], v[190:193], v[48:51]
	v_mfma_f32_16x16x32_bf16 v[40:43], v[174:177], v[224:227], v[40:43]
	v_mfma_f32_16x16x32_bf16 v[30:33], v[182:185], v[224:227], v[30:33]
	v_mfma_f32_16x16x32_bf16 v[22:25], v[174:177], v[238:241], v[22:25]
	v_mfma_f32_16x16x32_bf16 v[14:17], v[182:185], v[238:241], v[14:17]
	v_mfma_f32_16x16x32_bf16 v[6:9], v[174:177], v[246:249], v[6:9]
	v_mfma_f32_16x16x32_bf16 v[2:5], v[182:185], v[246:249], v[2:5]
	s_barrier
	s_add_i32 s52, s52, 2
	s_add_u32 s50, s50, 0x100
	s_addc_u32 s51, s51, 0
	s_add_u32 s34, s34, 0x100
	s_addc_u32 s35, s35, 0
	s_cmp_gt_u32 s52, 5
	s_cbranch_scc0 .LBB0_1199
	s_setprio 0
	s_and_b64 vcc, exec, s[22:23]
	s_cbranch_vccz .LBB0_1202
	s_barrier
